# cache-policy hint: nt on the read-once f32 weight loads of the weight-conversion loops (phase 0 and the conversions hosted in the layer-0 GEMM phases)
# speedup vs baseline: 1.0190x; 1.0190x over previous
; #define GAS __attribute__((address_space(1)))
; __device__ __forceinline__ void conv8_load(const ConvJob& J, int tid, f32x4 (&v)[16]) {
;     const int nblk = J.ncols / 256, k0 = 128 * (J.item / nblk), n0 = J.ncol0 + 256 * (J.item % nblk);
;     const int lane = tid & 63, w = tid >> 6, kg = lane & 7, nq = lane >> 3;
;     const GAS float* p = J.W + (size_t)(k0 + 16 * kg) * J.N + n0 + 32 * w + 4 * nq;
; #pragma unroll
;     for (int j = 0; j < 16; ++j) v[j] = *(const GAS f32x4*)(p + (size_t)j * J.N);
; }
;     ...
;     auto decode = [&](int it) -> ConvJob {
;         int r = it;
;         if (r < I_IN) return ConvJob{w_in, ws + WS_WIN, D_MODEL, IN_WIDTH, 1, r, 0, IN_WIDTH, 1, 64.f}; r -= I_IN;
;         if (r < I_INF) return ConvJob{w_in, ws + WS_WINF, D_MODEL, IN_WIDTH, 0, r, C_HF, HG_WIDTH, 0, 1.f}; r -= I_INF;
;         if (r < I_HG) return ConvJob{w_hg, ws + WS_WHG, HG_WIDTH, D_MODEL, 0, r, 0, D_MODEL, 0, 1.f}; r -= I_HG;
;         if (r < I_ATT) return ConvJob{w_att, ws + WS_WATT, ATT_OUT, D_MODEL, 0, r, 0, D_MODEL, 0, 1.f}; r -= I_ATT;
;         if (r < I_OUT) return ConvJob{w_out, ws + WS_WOUT, D_MODEL, D_MODEL, 0, r, 0, D_MODEL, 1, 64.f}; r -= I_OUT;
;         const int which = r / (NEXP1 * I_E); r -= which * (NEXP1 * I_E);
;         const int e = r / I_E, ri = r % I_E; const int es = gu8 ? 1 : 2;
;         if (which == 0) return ConvJob{(e < N_EXPERTS) ? w_eg + (size_t)e * D_MODEL * EXPERT_FF : w_sg, ws + (moe8 ? WS_WGU8 : WS_WGU) + (size_t)e * 1024 * D_MODEL * es, D_MODEL, EXPERT_FF, 2, ri, 0, EXPERT_FF, gu8 ? 1 : 0, 64.f};
;         if (which == 1) return ConvJob{(e < N_EXPERTS) ? w_eu + (size_t)e * D_MODEL * EXPERT_FF : w_su, ws + (moe8 ? WS_WGU8 : WS_WGU) + (size_t)e * 1024 * D_MODEL * es, D_MODEL, EXPERT_FF, 3, ri, 0, EXPERT_FF, gu8 ? 1 : 0, 64.f};
;         return ConvJob{(e < N_EXPERTS) ? w_ed + (size_t)e * EXPERT_FF * D_MODEL : w_sd, ws + (moe8 ? WS_WDN8 : WS_WDN) + (size_t)e * D_MODEL * EXPERT_FF, EXPERT_FF, D_MODEL, 0, ri, 0, D_MODEL, 1, 64.f};
.LBB0_29:
	v_cvt_f32_ubyte0_e32 v1, s21
	v_rcp_iflag_f32_e32 v1, v1
	s_sub_i32 s25, 0, s21
	s_abs_i32 s24, s1
	s_ashr_i32 s2, s1, 31
	v_mul_f32_e32 v1, 0x4f7ffffe, v1
	v_cvt_u32_f32_e32 v1, v1
	v_mov_b32_e32 v139, 0
	s_mov_b32 s15, 0
	v_mov_b32_e32 v133, v139
	v_readfirstlane_b32 s27, v1
	s_mul_i32 s25, s25, s27
	s_mul_hi_u32 s25, s27, s25
	s_add_i32 s27, s27, s25
	s_mul_hi_u32 s25, s24, s27
	s_mul_i32 s27, s25, s21
	s_sub_i32 s24, s24, s27
	s_add_i32 s28, s25, 1
	s_sub_i32 s27, s24, s21
	s_cmp_ge_u32 s24, s21
	s_cselect_b32 s25, s28, s25
	s_cselect_b32 s24, s27, s24
	s_add_i32 s27, s25, 1
	s_cmp_ge_u32 s24, s21
	s_cselect_b32 s24, s27, s25
	s_xor_b32 s24, s24, s2
	s_sub_i32 s24, s24, s2
	s_mul_i32 s2, s24, s21
	v_lshlrev_b32_e32 v1, 4, v130
	s_sub_i32 s1, s1, s2
	v_and_b32_e32 v132, 0x70, v1
	s_lshl_b32 s1, s1, 8
	v_lshl_or_b32 v1, s24, 7, v132
	s_add_i32 s2, s1, s3
	v_mad_i64_i32 v[2:3], s[24:25], s14, v1, 0
	v_ashrrev_i32_e32 v1, 1, v130
	v_lshl_add_u64 v[2:3], v[2:3], 2, s[4:5]
	s_ashr_i32 s3, s2, 31
	v_and_b32_e32 v134, 0xffffffe0, v1
	v_lshrrev_b32_e32 v1, 1, v130
	v_lshl_add_u64 v[2:3], s[2:3], 2, v[2:3]
	v_ashrrev_i32_e32 v135, 31, v134
	v_and_b32_e32 v136, 28, v1
	v_lshl_add_u64 v[2:3], v[134:135], 2, v[2:3]
	v_lshlrev_b32_e32 v138, 2, v136
	v_lshl_add_u64 v[10:11], v[2:3], 0, v[138:139]
	s_lshl_b32 s14, s14, 2
	v_lshl_add_u64 v[12:13], v[10:11], 0, s[14:15]
	v_lshl_add_u64 v[18:19], v[12:13], 0, s[14:15]
	v_lshl_add_u64 v[20:21], v[18:19], 0, s[14:15]
	v_lshl_add_u64 v[26:27], v[20:21], 0, s[14:15]
	v_lshl_add_u64 v[28:29], v[26:27], 0, s[14:15]
	v_lshl_add_u64 v[30:31], v[28:29], 0, s[14:15]
	v_lshl_add_u64 v[34:35], v[30:31], 0, s[14:15]
	v_lshl_add_u64 v[38:39], v[34:35], 0, s[14:15]
	v_lshl_add_u64 v[42:43], v[38:39], 0, s[14:15]
	v_lshl_add_u64 v[46:47], v[42:43], 0, s[14:15]
	global_load_dwordx4 v[2:5], v[10:11], off nt
	global_load_dwordx4 v[6:9], v[12:13], off nt
	s_nop 0
	global_load_dwordx4 v[10:13], v[18:19], off nt
	global_load_dwordx4 v[14:17], v[20:21], off nt
	s_nop 0
	global_load_dwordx4 v[18:21], v[26:27], off nt
	global_load_dwordx4 v[22:25], v[28:29], off nt
	s_add_u32 s28, s18, 0x3c00000
	global_load_dwordx4 v[26:29], v[30:31], off nt
	s_addc_u32 s29, s19, 0
	global_load_dwordx4 v[30:33], v[34:35], off nt
	s_add_u32 s30, s18, 0x3a00000
	global_load_dwordx4 v[34:37], v[38:39], off nt
	s_addc_u32 s31, s19, 0
	global_load_dwordx4 v[38:41], v[42:43], off nt
	s_add_u32 s34, s18, 0x3600000
	global_load_dwordx4 v[42:45], v[46:47], off nt
	v_lshl_add_u64 v[46:47], v[46:47], 0, s[14:15]
	v_lshl_add_u64 v[50:51], v[46:47], 0, s[14:15]
	v_lshl_add_u64 v[54:55], v[50:51], 0, s[14:15]
	v_lshl_add_u64 v[56:57], v[54:55], 0, s[14:15]
	global_load_dwordx4 v[46:49], v[46:47], off nt
	s_movk_i32 s1, 0x7c
	global_load_dwordx4 v[50:53], v[50:51], off nt
	s_addc_u32 s35, s19, 0
	global_load_dwordx4 v[62:65], v[54:55], off nt
	v_lshl_add_u64 v[54:55], v[56:57], 0, s[14:15]
	global_load_dwordx4 v[70:73], v[56:57], off nt
	global_load_dwordx4 v[78:81], v[54:55], off nt
	v_bitop3_b32 v1, v136, s1, v134 bitop3:0xc8
	s_add_u32 s36, s18, 0x2200000
	v_lshlrev_b32_e32 v54, 1, v1
	s_addc_u32 s37, s19, 0
	v_add_u32_e32 v55, 0xffffff81, v54
	v_cmp_gt_u32_e32 vcc, 64, v1
	s_add_u32 s38, s18, 0x400000
	v_or_b32_e32 v131, v136, v134
	v_cndmask_b32_e32 v1, v55, v54, vcc
	s_addc_u32 s39, s19, 0
	s_lshl_b32 s1, s20, 1
	s_movk_i32 s2, 0xc00
	s_mov_b32 s21, s26
	s_branch .LBB0_32

; #define GAS __attribute__((address_space(1)))
; __device__ __forceinline__ void conv8_load(const ConvJob& J, int tid, f32x4 (&v)[16]) {
;     const int nblk = J.ncols / 256, k0 = 128 * (J.item / nblk), n0 = J.ncol0 + 256 * (J.item % nblk);
;     const int lane = tid & 63, w = tid >> 6, kg = lane & 7, nq = lane >> 3;
;     const GAS float* p = J.W + (size_t)(k0 + 16 * kg) * J.N + n0 + 32 * w + 4 * nq;
; #pragma unroll
;     for (int j = 0; j < 16; ++j) v[j] = *(const GAS f32x4*)(p + (size_t)j * J.N);
; }
;     ...
;                 const int q1 = q + F.G; const bool m1 = q1 < q_hi;
;                 if (m1) conv8_load(decode(q1 < I_IN ? q1 : q1 + NB16), tid, vb);
.LBB0_49:
	v_cvt_f32_ubyte0_e32 v54, s27
	v_rcp_iflag_f32_e32 v54, v54
	s_sub_i32 s43, 0, s27
	s_abs_i32 s33, s14
	s_ashr_i32 s24, s14, 31
	v_mul_f32_e32 v54, 0x4f7ffffe, v54
	v_cvt_u32_f32_e32 v54, v54
	v_lshlrev_b32_e32 v138, 2, v136
	v_readfirstlane_b32 s44, v54
	s_mul_i32 s43, s43, s44
	s_mul_hi_u32 s43, s44, s43
	s_add_i32 s44, s44, s43
	s_mul_hi_u32 s43, s33, s44
	s_mul_i32 s44, s43, s27
	s_sub_i32 s33, s33, s44
	s_add_i32 s45, s43, 1
	s_sub_i32 s44, s33, s27
	s_cmp_ge_u32 s33, s27
	s_cselect_b32 s43, s45, s43
	s_cselect_b32 s33, s44, s33
	s_add_i32 s44, s43, 1
	s_cmp_ge_u32 s33, s27
	s_cselect_b32 s33, s44, s43
	s_xor_b32 s33, s33, s24
	s_sub_i32 s24, s33, s24
	s_mul_i32 s27, s24, s27
	s_sub_i32 s14, s14, s27
	v_lshl_or_b32 v54, s24, 7, v132
	s_lshl_b32 s14, s14, 8
	s_add_i32 s24, s14, s25
	v_mad_i64_i32 v[54:55], s[44:45], s42, v54, 0
	v_lshl_add_u64 v[54:55], v[54:55], 2, s[4:5]
	s_ashr_i32 s25, s24, 31
	v_lshl_add_u64 v[54:55], s[24:25], 2, v[54:55]
	v_lshl_add_u64 v[54:55], v[134:135], 2, v[54:55]
	v_lshl_add_u64 v[54:55], v[54:55], 0, v[138:139]
	s_lshl_b32 s14, s42, 2
	v_lshl_add_u64 v[66:67], v[54:55], 0, s[14:15]
	global_load_dwordx4 v[54:57], v[54:55], off nt
	s_nop 0
	global_load_dwordx4 v[58:61], v[66:67], off nt
	v_lshl_add_u64 v[66:67], v[66:67], 0, s[14:15]
	v_lshl_add_u64 v[82:83], v[66:67], 0, s[14:15]
	global_load_dwordx4 v[66:69], v[66:67], off nt
	s_nop 0
	global_load_dwordx4 v[74:77], v[82:83], off nt
	v_lshl_add_u64 v[82:83], v[82:83], 0, s[14:15]
	v_lshl_add_u64 v[90:91], v[82:83], 0, s[14:15]
	v_lshl_add_u64 v[94:95], v[90:91], 0, s[14:15]
	v_lshl_add_u64 v[98:99], v[94:95], 0, s[14:15]
	v_lshl_add_u64 v[102:103], v[98:99], 0, s[14:15]
	v_lshl_add_u64 v[106:107], v[102:103], 0, s[14:15]
	v_lshl_add_u64 v[110:111], v[106:107], 0, s[14:15]
	v_lshl_add_u64 v[114:115], v[110:111], 0, s[14:15]
	v_lshl_add_u64 v[118:119], v[114:115], 0, s[14:15]
	v_lshl_add_u64 v[122:123], v[118:119], 0, s[14:15]
	v_lshl_add_u64 v[126:127], v[122:123], 0, s[14:15]
	global_load_dwordx4 v[82:85], v[82:83], off nt
	s_nop 0
	global_load_dwordx4 v[86:89], v[90:91], off nt
	s_nop 0
	global_load_dwordx4 v[90:93], v[94:95], off nt
	s_nop 0
	global_load_dwordx4 v[94:97], v[98:99], off nt
	s_nop 0
	global_load_dwordx4 v[98:101], v[102:103], off nt
	s_nop 0
	global_load_dwordx4 v[102:105], v[106:107], off nt
	s_nop 0
	global_load_dwordx4 v[106:109], v[110:111], off nt
	s_nop 0
	global_load_dwordx4 v[110:113], v[114:115], off nt
	s_nop 0
	global_load_dwordx4 v[114:117], v[118:119], off nt
	s_nop 0
	global_load_dwordx4 v[118:121], v[122:123], off nt
	s_nop 0
	global_load_dwordx4 v[122:125], v[126:127], off nt
	v_lshl_add_u64 v[126:127], v[126:127], 0, s[14:15]
	global_load_dwordx4 v[126:129], v[126:127], off nt

; #define GAS __attribute__((address_space(1)))
; __device__ __forceinline__ void conv8_load(const ConvJob& J, int tid, f32x4 (&v)[16]) {
;     const int nblk = J.ncols / 256, k0 = 128 * (J.item / nblk), n0 = J.ncol0 + 256 * (J.item % nblk);
;     const int lane = tid & 63, w = tid >> 6, kg = lane & 7, nq = lane >> 3;
;     const GAS float* p = J.W + (size_t)(k0 + 16 * kg) * J.N + n0 + 32 * w + 4 * nq;
; #pragma unroll
;     for (int j = 0; j < 16; ++j) v[j] = *(const GAS f32x4*)(p + (size_t)j * J.N);
; }
;     ...
;                 const int q2 = q1 + F.G; const bool m2 = q2 < q_hi;
;                 if (m2) conv8_load(decode(q2 < I_IN ? q2 : q2 + NB16), tid, va);
.LBB0_90:
	v_cvt_f32_ubyte0_e32 v2, s25
	v_rcp_iflag_f32_e32 v2, v2
	s_sub_i32 s33, 0, s25
	s_abs_i32 s27, s14
	s_ashr_i32 s21, s14, 31
	v_mul_f32_e32 v2, 0x4f7ffffe, v2
	v_cvt_u32_f32_e32 v2, v2
	v_lshlrev_b32_e32 v138, 2, v136
	v_readfirstlane_b32 s41, v2
	s_mul_i32 s33, s33, s41
	s_mul_hi_u32 s33, s41, s33
	s_add_i32 s41, s41, s33
	s_mul_hi_u32 s33, s27, s41
	s_mul_i32 s41, s33, s25
	s_sub_i32 s27, s27, s41
	s_add_i32 s42, s33, 1
	s_sub_i32 s41, s27, s25
	s_cmp_ge_u32 s27, s25
	s_cselect_b32 s33, s42, s33
	s_cselect_b32 s27, s41, s27
	s_add_i32 s41, s33, 1
	s_cmp_ge_u32 s27, s25
	s_cselect_b32 s27, s41, s33
	s_xor_b32 s27, s27, s21
	s_sub_i32 s21, s27, s21
	s_mul_i32 s25, s21, s25
	s_sub_i32 s14, s14, s25
	v_lshl_or_b32 v2, s21, 7, v132
	s_lshl_b32 s14, s14, 8
	s_add_i32 s24, s14, s24
	v_mad_i64_i32 v[2:3], s[42:43], s40, v2, 0
	v_lshl_add_u64 v[2:3], v[2:3], 2, s[4:5]
	s_ashr_i32 s25, s24, 31
	v_lshl_add_u64 v[2:3], s[24:25], 2, v[2:3]
	v_lshl_add_u64 v[2:3], v[134:135], 2, v[2:3]
	v_lshl_add_u64 v[10:11], v[2:3], 0, v[138:139]
	s_lshl_b32 s14, s40, 2
	v_lshl_add_u64 v[12:13], v[10:11], 0, s[14:15]
	v_lshl_add_u64 v[18:19], v[12:13], 0, s[14:15]
	v_lshl_add_u64 v[20:21], v[18:19], 0, s[14:15]
	v_lshl_add_u64 v[26:27], v[20:21], 0, s[14:15]
	v_lshl_add_u64 v[28:29], v[26:27], 0, s[14:15]
	v_lshl_add_u64 v[30:31], v[28:29], 0, s[14:15]
	v_lshl_add_u64 v[34:35], v[30:31], 0, s[14:15]
	v_lshl_add_u64 v[38:39], v[34:35], 0, s[14:15]
	v_lshl_add_u64 v[42:43], v[38:39], 0, s[14:15]
	v_lshl_add_u64 v[46:47], v[42:43], 0, s[14:15]
	v_lshl_add_u64 v[50:51], v[46:47], 0, s[14:15]
	v_lshl_add_u64 v[62:63], v[50:51], 0, s[14:15]
	v_lshl_add_u64 v[70:71], v[62:63], 0, s[14:15]
	v_lshl_add_u64 v[78:79], v[70:71], 0, s[14:15]
	global_load_dwordx4 v[2:5], v[10:11], off nt
	global_load_dwordx4 v[6:9], v[12:13], off nt
	s_nop 0
	global_load_dwordx4 v[10:13], v[18:19], off nt
	global_load_dwordx4 v[14:17], v[20:21], off nt
	s_nop 0
	global_load_dwordx4 v[18:21], v[26:27], off nt
	global_load_dwordx4 v[22:25], v[28:29], off nt
	s_nop 0
	global_load_dwordx4 v[26:29], v[30:31], off nt
	s_nop 0
	global_load_dwordx4 v[30:33], v[34:35], off nt
	s_nop 0
	global_load_dwordx4 v[34:37], v[38:39], off nt
	s_nop 0
	global_load_dwordx4 v[38:41], v[42:43], off nt
	s_nop 0
	global_load_dwordx4 v[42:45], v[46:47], off nt
	s_nop 0
	global_load_dwordx4 v[46:49], v[50:51], off nt
	s_nop 0
	global_load_dwordx4 v[50:53], v[62:63], off nt
	s_nop 0
	global_load_dwordx4 v[62:65], v[70:71], off nt
	s_nop 0
	global_load_dwordx4 v[70:73], v[78:79], off nt
	v_lshl_add_u64 v[78:79], v[78:79], 0, s[14:15]
	global_load_dwordx4 v[78:81], v[78:79], off nt

; #define GAS __attribute__((address_space(1)))
; #define LAS __attribute__((address_space(3)))
; __device__ __forceinline__ void conv_load(const ConvJob& J, int tid, f32x4 (&v)[16]) {
;     const int nblk = J.ncols / 256, k0 = 128 * (J.item / nblk), n0 = J.ncol0 + 256 * (J.item % nblk);
;     {
; #pragma unroll
;         for (int ii = 0; ii < 16; ++ii) { const int idx = tid + 512 * ii, k = idx >> 6, c4 = idx & 63; v[ii] = *(const GAS f32x4*)(J.W + (size_t)(k0 + k) * J.N + n0 + 4 * c4); }
;     }
; }
; __device__ __forceinline__ void conv_to_lds(const ConvJob& J, int tid, const f32x4 (&v)[16], LAS float* T) {
; #pragma unroll
;     for (int ii = 0; ii < 16; ++ii) { const int idx = tid + 512 * ii, k = idx >> 6, c4 = idx & 63; const int g = J.f8 ? ((k >> 4) & 7) : ((k >> 3) & 15);
;         *(LAS f32x4*)(T + k * 256 + 4 * (c4 ^ g)) = v[ii]; }
; }
.LBB0_126:
	v_cvt_f32_ubyte0_e32 v115, s24
	v_rcp_iflag_f32_e32 v115, v115
	s_sub_i32 s34, 0, s24
	s_abs_i32 s33, s21
	s_ashr_i32 s27, s21, 31
	v_mul_f32_e32 v115, 0x4f7ffffe, v115
	v_cvt_u32_f32_e32 v115, v115
	v_xor_b32_e32 v114, v114, v1
	v_xor_b32_e32 v113, v113, v1
	v_xor_b32_e32 v112, v112, v1
	v_readfirstlane_b32 s35, v115
	s_mul_i32 s34, s34, s35
	s_mul_hi_u32 s34, s35, s34
	s_add_i32 s35, s35, s34
	s_mul_hi_u32 s34, s33, s35
	s_mul_i32 s35, s34, s24
	s_sub_i32 s33, s33, s35
	s_add_i32 s43, s34, 1
	s_sub_i32 s35, s33, s24
	s_cmp_ge_u32 s33, s24
	s_cselect_b32 s34, s43, s34
	s_cselect_b32 s33, s35, s33
	s_add_i32 s35, s34, 1
	s_cmp_ge_u32 s33, s24
	s_cselect_b32 s33, s35, s34
	s_xor_b32 s33, s33, s27
	s_sub_i32 s27, s33, s27
	s_lshl_b32 s34, s27, 7
	s_mul_i32 s27, s27, s24
	s_sub_i32 s21, s21, s27
	s_lshl_b32 s21, s21, 8
	s_add_i32 s24, s21, s25
	v_add_u32_e32 v115, s34, v5
	s_ashr_i32 s25, s24, 31
	v_mad_i64_i32 v[116:117], s[44:45], s42, v115, 0
	v_add_u32_e32 v115, s34, v10
	s_lshl_b64 s[44:45], s[24:25], 2
	v_mad_i64_i32 v[118:119], s[24:25], s42, v115, 0
	v_add_u32_e32 v115, s34, v11
	v_mad_i64_i32 v[124:125], s[24:25], s42, v115, 0
	v_add_u32_e32 v115, s34, v12
	v_mad_i64_i32 v[126:127], s[24:25], s42, v115, 0
	v_lshl_add_u64 v[116:117], v[116:117], 2, s[40:41]
	v_lshl_add_u64 v[118:119], v[118:119], 2, s[40:41]
	v_lshl_add_u64 v[124:125], v[124:125], 2, s[40:41]
	v_lshl_add_u64 v[126:127], v[126:127], 2, s[40:41]
	v_lshl_add_u64 v[116:117], v[116:117], 0, s[44:45]
	v_lshl_add_u64 v[118:119], v[118:119], 0, s[44:45]
	v_lshl_add_u64 v[124:125], v[124:125], 0, s[44:45]
	v_lshl_add_u64 v[126:127], v[126:127], 0, s[44:45]
	v_lshl_add_u64 v[116:117], v[116:117], 0, v[2:3]
	v_lshl_add_u64 v[120:121], v[118:119], 0, v[2:3]
	v_lshl_add_u64 v[124:125], v[124:125], 0, v[2:3]
	v_lshl_add_u64 v[128:129], v[126:127], 0, v[2:3]
	v_add_u32_e32 v115, s34, v13
	global_load_dwordx4 v[116:119], v[116:117], off nt
	s_nop 0
	global_load_dwordx4 v[120:123], v[120:121], off nt
	s_nop 0
	global_load_dwordx4 v[124:127], v[124:125], off nt
	s_nop 0
	global_load_dwordx4 v[132:135], v[128:129], off nt
	v_mad_i64_i32 v[128:129], s[24:25], s42, v115, 0
	v_add_u32_e32 v115, s34, v14
	v_mad_i64_i32 v[136:137], s[24:25], s42, v115, 0
	v_lshl_add_u64 v[128:129], v[128:129], 2, s[40:41]
	v_lshl_add_u64 v[136:137], v[136:137], 2, s[40:41]
	v_lshl_add_u64 v[128:129], v[128:129], 0, s[44:45]
	v_lshl_add_u64 v[136:137], v[136:137], 0, s[44:45]
	v_lshl_add_u64 v[128:129], v[128:129], 0, v[2:3]
	v_lshl_add_u64 v[140:141], v[136:137], 0, v[2:3]
	v_add_u32_e32 v115, s34, v15
	global_load_dwordx4 v[136:139], v[128:129], off nt
	s_nop 0
	global_load_dwordx4 v[140:143], v[140:141], off nt
	v_mad_i64_i32 v[128:129], s[24:25], s42, v115, 0
	v_add_u32_e32 v115, s34, v16
	v_mad_i64_i32 v[144:145], s[24:25], s42, v115, 0
	v_lshl_add_u64 v[128:129], v[128:129], 2, s[40:41]
	v_lshl_add_u64 v[144:145], v[144:145], 2, s[40:41]
	v_lshl_add_u64 v[128:129], v[128:129], 0, s[44:45]
	v_lshl_add_u64 v[144:145], v[144:145], 0, s[44:45]
	v_lshl_add_u64 v[128:129], v[128:129], 0, v[2:3]
	v_lshl_add_u64 v[148:149], v[144:145], 0, v[2:3]
	v_add_u32_e32 v115, s34, v17
	global_load_dwordx4 v[144:147], v[128:129], off nt
	s_nop 0
	global_load_dwordx4 v[148:151], v[148:149], off nt
	v_mad_i64_i32 v[128:129], s[24:25], s42, v115, 0
	v_add_u32_e32 v115, s34, v18
	v_mad_i64_i32 v[152:153], s[24:25], s42, v115, 0
	v_lshl_add_u64 v[128:129], v[128:129], 2, s[40:41]
	v_lshl_add_u64 v[152:153], v[152:153], 2, s[40:41]
	v_lshl_add_u64 v[128:129], v[128:129], 0, s[44:45]
	v_lshl_add_u64 v[152:153], v[152:153], 0, s[44:45]
	v_lshl_add_u64 v[128:129], v[128:129], 0, v[2:3]
	v_lshl_add_u64 v[156:157], v[152:153], 0, v[2:3]
	v_add_u32_e32 v115, s34, v19
	global_load_dwordx4 v[152:155], v[128:129], off nt
	s_nop 0
	global_load_dwordx4 v[156:159], v[156:157], off nt
	v_mad_i64_i32 v[128:129], s[24:25], s42, v115, 0
	v_add_u32_e32 v115, s34, v20
	v_mad_i64_i32 v[160:161], s[24:25], s42, v115, 0
	v_lshl_add_u64 v[128:129], v[128:129], 2, s[40:41]
	v_lshl_add_u64 v[160:161], v[160:161], 2, s[40:41]
	v_lshl_add_u64 v[128:129], v[128:129], 0, s[44:45]
	v_lshl_add_u64 v[160:161], v[160:161], 0, s[44:45]
	v_lshl_add_u64 v[128:129], v[128:129], 0, v[2:3]
	v_lshl_add_u64 v[164:165], v[160:161], 0, v[2:3]
	v_add_u32_e32 v115, s34, v21
	global_load_dwordx4 v[160:163], v[128:129], off nt
	s_nop 0
	global_load_dwordx4 v[164:167], v[164:165], off nt
	v_mad_i64_i32 v[128:129], s[24:25], s42, v115, 0
	v_add_u32_e32 v115, s34, v22
	v_mad_i64_i32 v[168:169], s[24:25], s42, v115, 0
	v_lshl_add_u64 v[128:129], v[128:129], 2, s[40:41]
	v_lshl_add_u64 v[168:169], v[168:169], 2, s[40:41]
	v_lshl_add_u64 v[128:129], v[128:129], 0, s[44:45]
	v_lshl_add_u64 v[168:169], v[168:169], 0, s[44:45]
	v_lshl_add_u64 v[128:129], v[128:129], 0, v[2:3]
	v_lshl_add_u64 v[172:173], v[168:169], 0, v[2:3]
	v_add_u32_e32 v115, s34, v23
	global_load_dwordx4 v[168:171], v[128:129], off nt
	s_nop 0
	global_load_dwordx4 v[172:175], v[172:173], off nt
	v_mad_i64_i32 v[128:129], s[24:25], s42, v115, 0
	v_lshl_add_u64 v[128:129], v[128:129], 2, s[40:41]
	v_lshl_add_u64 v[128:129], v[128:129], 0, s[44:45]
	v_lshl_add_u64 v[128:129], v[128:129], 0, v[2:3]
	v_add_u32_e32 v115, s34, v24
	global_load_dwordx4 v[176:179], v[128:129], off nt
	v_mad_i64_i32 v[128:129], s[24:25], s42, v115, 0
	v_lshl_add_u64 v[128:129], v[128:129], 2, s[40:41]
	v_lshl_add_u64 v[128:129], v[128:129], 0, s[44:45]
	v_lshl_add_u64 v[128:129], v[128:129], 0, v[2:3]
	global_load_dwordx4 v[180:183], v[128:129], off nt
	v_xor_b32_e32 v111, v111, v1
	v_xor_b32_e32 v110, v110, v1
	v_xor_b32_e32 v109, v109, v1
	v_xor_b32_e32 v108, v108, v1
	v_xor_b32_e32 v107, v107, v1
	v_xor_b32_e32 v106, v106, v1
	v_xor_b32_e32 v105, v105, v1
	v_xor_b32_e32 v104, v104, v1
	v_xor_b32_e32 v103, v103, v1
	v_xor_b32_e32 v102, v102, v1
	v_xor_b32_e32 v101, v101, v1
	v_xor_b32_e32 v9, v9, v1
	v_xor_b32_e32 v8, v8, v1
	v_lshl_add_u32 v114, v114, 4, v27
	v_lshl_add_u32 v113, v113, 4, v30
	v_lshl_add_u32 v112, v112, 4, v33
	v_lshl_add_u32 v111, v111, 4, v36
	v_lshl_add_u32 v110, v110, 4, v39
	v_lshl_add_u32 v109, v109, 4, v42
	v_lshl_add_u32 v108, v108, 4, v45
	v_lshl_add_u32 v107, v107, 4, v48
	v_lshl_add_u32 v106, v106, 4, v51
	v_lshl_add_u32 v105, v105, 4, v54
	v_lshl_add_u32 v104, v104, 4, v57
	v_lshl_add_u32 v103, v103, 4, v60
	v_lshl_add_u32 v102, v102, 4, v63
	v_lshl_add_u32 v101, v101, 4, v66
	v_lshl_add_u32 v9, v9, 4, v69
	v_lshl_add_u32 v8, v8, 4, v72
	s_waitcnt vmcnt(15)
; #define LAS __attribute__((address_space(3)))
; #define LDS_BARRIER() asm volatile("s_waitcnt lgkmcnt(0)\n\ts_barrier" ::: "memory")
; __device__ __forceinline__ void conv_to_lds(const ConvJob& J, int tid, const f32x4 (&v)[16], LAS float* T) {
; #pragma unroll
;     for (int ii = 0; ii < 16; ++ii) { const int idx = tid + 512 * ii, k = idx >> 6, c4 = idx & 63; const int g = J.f8 ? ((k >> 4) & 7) : ((k >> 3) & 15);
;         *(LAS f32x4*)(T + k * 256 + 4 * (c4 ^ g)) = v[ii]; }
; }
;     ...
;             for (int it = I_IN + (F.G - 1 - F.bid); it < I_IN + NB16; it += F.G) { const ConvJob j = decode(it); f32x4 v[16];
;                 conv_load(j, tid, v); conv_to_lds(j, tid, v, TL); LDS_BARRIER(); conv_from_lds(j, tid, TL); LDS_BARRIER(); }
	ds_write_b128 v114, v[116:119]
	s_waitcnt vmcnt(14)
	ds_write_b128 v113, v[120:123]
	s_waitcnt vmcnt(13)
	ds_write_b128 v112, v[124:127]
	s_waitcnt vmcnt(12)
	ds_write_b128 v111, v[132:135]
	s_waitcnt vmcnt(11)
	ds_write_b128 v110, v[136:139]
	s_waitcnt vmcnt(10)
	ds_write_b128 v109, v[140:143]
	s_waitcnt vmcnt(9)
	ds_write_b128 v108, v[144:147]
	s_waitcnt vmcnt(8)
	ds_write_b128 v107, v[148:151]
	s_ashr_i32 s35, s34, 31
	s_mov_b64 s[40:41], -1
	s_waitcnt vmcnt(7)
	ds_write_b128 v106, v[152:155]
	s_waitcnt vmcnt(6)
	ds_write_b128 v105, v[156:159]
	s_and_b64 vcc, exec, s[38:39]
	s_waitcnt vmcnt(5)
	ds_write_b128 v104, v[160:163]
	s_waitcnt vmcnt(4)
	ds_write_b128 v103, v[164:167]
	s_waitcnt vmcnt(3)
	ds_write_b128 v102, v[168:171]
	s_waitcnt vmcnt(2)
	ds_write_b128 v101, v[172:175]
	s_waitcnt vmcnt(1)
	ds_write_b128 v9, v[176:179]
	s_waitcnt vmcnt(0)
	ds_write_b128 v8, v[180:183]
	s_waitcnt lgkmcnt(0)
	s_barrier
	s_cbranch_vccz .LBB0_128
; #define GAS __attribute__((address_space(1)))
; #define LAS __attribute__((address_space(3)))
; __device__ __forceinline__ unsigned cvt_pk_bf16(float lo, float hi) { unsigned r; asm volatile("v_cvt_pk_bf16_f32 %0, %1, %2" : "=v"(r) : "v"(lo), "v"(hi)); return r; }
; __device__ __forceinline__ int conv_dst_row(int mode, int n) {
;     if (mode == 1) { if (n >= C_AQ && n < C_AV) { const int hb = n & ~127, dd = n & 127; return hb + (dd < 64 ? 2 * dd : 2 * (dd - 64) + 1); } return n; }
;     if (mode == 2) return (n >> 7) * 256 + (n & 127);
;     if (mode == 3) return (n >> 7) * 256 + 128 + (n & 127);
;     return n;
; }
; __device__ __forceinline__ void conv_from_lds(const ConvJob& J, int tid, const LAS float* T) {
;     ...
;         const int c = ((lane >> 2) & 7) + 8 * (lane >> 5);
; #pragma unroll
;         for (int it = 0; it < 8; ++it) { const int c4n = w * 8 + it, n = 4 * c4n + j; const LAS float* base = T + 4 * (c4n ^ c) + j + (8 * c) * 256;
;             u32x4 o; o.x = cvt_pk_bf16(base[0 * 256], base[1 * 256]); o.y = cvt_pk_bf16(base[2 * 256], base[3 * 256]); o.z = cvt_pk_bf16(base[4 * 256], base[5 * 256]); o.w = cvt_pk_bf16(base[6 * 256], base[7 * 256]);
;             *(GAS u32x4*)(J.WT + ((size_t)conv_dst_row(J.mode, n0 - J.ncol0 + n) * J.K + k0 + 8 * c) * 2) = o; }
	ds_read2st64_b32 v[8:9], v89 offset1:4
	s_waitcnt lgkmcnt(0)
	v_cvt_pk_bf16_f32 v102, v8, v9
	ds_read2st64_b32 v[8:9], v89 offset0:8 offset1:12
	v_add_u32_e32 v101, s21, v73
	s_waitcnt lgkmcnt(0)
	v_cvt_pk_bf16_f32 v103, v8, v9
	v_mov_b32_e32 v9, s35
	v_or_b32_e32 v8, s34, v4
	v_ashrrev_i32_e32 v110, 31, v101
	v_mad_u64_u32 v[108:109], s[24:25], s30, v101, v[8:9]
	v_mul_lo_u32 v101, s31, v101
	v_mul_lo_u32 v110, s30, v110
	ds_read2st64_b32 v[104:105], v89 offset0:16 offset1:20
	v_add3_u32 v109, v101, v109, v110
	v_add_u32_e32 v101, s21, v74
	s_waitcnt lgkmcnt(0)
	v_cvt_pk_bf16_f32 v104, v104, v105
	ds_read2st64_b32 v[106:107], v89 offset0:24 offset1:28
	s_waitcnt lgkmcnt(0)
	v_cvt_pk_bf16_f32 v105, v106, v107
	v_lshl_add_u64 v[108:109], v[108:109], 1, s[36:37]
	v_ashrrev_i32_e32 v110, 31, v101
	ds_read2st64_b32 v[106:107], v90 offset1:4
	global_store_dwordx4 v[108:109], v[102:105], off
	v_mad_u64_u32 v[108:109], s[24:25], s30, v101, v[8:9]
	s_waitcnt lgkmcnt(0)
	v_cvt_pk_bf16_f32 v102, v106, v107
	ds_read2st64_b32 v[104:105], v90 offset0:8 offset1:12
	v_mul_lo_u32 v101, s31, v101
	v_mul_lo_u32 v110, s30, v110
	s_waitcnt lgkmcnt(0)
	v_cvt_pk_bf16_f32 v103, v104, v105
	ds_read2st64_b32 v[104:105], v90 offset0:16 offset1:20
	v_add3_u32 v109, v101, v109, v110
	v_add_u32_e32 v101, s21, v75
	s_waitcnt lgkmcnt(0)
	v_cvt_pk_bf16_f32 v104, v104, v105
	ds_read2st64_b32 v[106:107], v90 offset0:24 offset1:28
	s_waitcnt lgkmcnt(0)
	v_cvt_pk_bf16_f32 v105, v106, v107
	v_lshl_add_u64 v[108:109], v[108:109], 1, s[36:37]
	v_ashrrev_i32_e32 v110, 31, v101
	ds_read2st64_b32 v[106:107], v91 offset1:4
	global_store_dwordx4 v[108:109], v[102:105], off
	v_mad_u64_u32 v[108:109], s[24:25], s30, v101, v[8:9]
	s_waitcnt lgkmcnt(0)
	v_cvt_pk_bf16_f32 v102, v106, v107
	ds_read2st64_b32 v[104:105], v91 offset0:8 offset1:12
	v_mul_lo_u32 v101, s31, v101
	v_mul_lo_u32 v110, s30, v110
	s_waitcnt lgkmcnt(0)
	v_cvt_pk_bf16_f32 v103, v104, v105
	ds_read2st64_b32 v[104:105], v91 offset0:16 offset1:20
	v_add3_u32 v109, v101, v109, v110
	v_add_u32_e32 v101, s21, v76
	s_waitcnt lgkmcnt(0)
	v_cvt_pk_bf16_f32 v104, v104, v105
	ds_read2st64_b32 v[106:107], v91 offset0:24 offset1:28
	s_waitcnt lgkmcnt(0)
	v_cvt_pk_bf16_f32 v105, v106, v107
	v_lshl_add_u64 v[108:109], v[108:109], 1, s[36:37]
	v_ashrrev_i32_e32 v110, 31, v101
	ds_read2st64_b32 v[106:107], v92 offset1:4
	global_store_dwordx4 v[108:109], v[102:105], off
	v_mad_u64_u32 v[108:109], s[24:25], s30, v101, v[8:9]
	s_waitcnt lgkmcnt(0)
	v_cvt_pk_bf16_f32 v102, v106, v107
	ds_read2st64_b32 v[104:105], v92 offset0:8 offset1:12
	v_mul_lo_u32 v101, s31, v101
	v_mul_lo_u32 v110, s30, v110
	s_waitcnt lgkmcnt(0)
	v_cvt_pk_bf16_f32 v103, v104, v105
	ds_read2st64_b32 v[104:105], v92 offset0:16 offset1:20
	v_add3_u32 v109, v101, v109, v110
	v_add_u32_e32 v101, s21, v77
	s_waitcnt lgkmcnt(0)
	v_cvt_pk_bf16_f32 v104, v104, v105
	ds_read2st64_b32 v[106:107], v92 offset0:24 offset1:28
	s_waitcnt lgkmcnt(0)
	v_cvt_pk_bf16_f32 v105, v106, v107
	v_lshl_add_u64 v[108:109], v[108:109], 1, s[36:37]
	v_ashrrev_i32_e32 v110, 31, v101
	ds_read2st64_b32 v[106:107], v93 offset1:4
	global_store_dwordx4 v[108:109], v[102:105], off
	v_mad_u64_u32 v[108:109], s[24:25], s30, v101, v[8:9]
	s_waitcnt lgkmcnt(0)
	v_cvt_pk_bf16_f32 v102, v106, v107
	ds_read2st64_b32 v[104:105], v93 offset0:8 offset1:12
	v_mul_lo_u32 v101, s31, v101
	v_mul_lo_u32 v110, s30, v110
	s_waitcnt lgkmcnt(0)
	v_cvt_pk_bf16_f32 v103, v104, v105
	ds_read2st64_b32 v[104:105], v93 offset0:16 offset1:20
	v_add3_u32 v109, v101, v109, v110
	v_add_u32_e32 v101, s21, v78
	s_waitcnt lgkmcnt(0)
	v_cvt_pk_bf16_f32 v104, v104, v105
	ds_read2st64_b32 v[106:107], v93 offset0:24 offset1:28
	s_waitcnt lgkmcnt(0)
	v_cvt_pk_bf16_f32 v105, v106, v107
	v_lshl_add_u64 v[108:109], v[108:109], 1, s[36:37]
	v_ashrrev_i32_e32 v110, 31, v101
	ds_read2st64_b32 v[106:107], v94 offset1:4
	global_store_dwordx4 v[108:109], v[102:105], off
	v_mad_u64_u32 v[108:109], s[24:25], s30, v101, v[8:9]
	s_waitcnt lgkmcnt(0)
	v_cvt_pk_bf16_f32 v102, v106, v107
	ds_read2st64_b32 v[104:105], v94 offset0:8 offset1:12
	v_mul_lo_u32 v101, s31, v101
	v_mul_lo_u32 v110, s30, v110
	s_waitcnt lgkmcnt(0)
	v_cvt_pk_bf16_f32 v103, v104, v105
	ds_read2st64_b32 v[104:105], v94 offset0:16 offset1:20
	v_add3_u32 v109, v101, v109, v110
	v_add_u32_e32 v101, s21, v79
	s_waitcnt lgkmcnt(0)
	v_cvt_pk_bf16_f32 v104, v104, v105
	ds_read2st64_b32 v[106:107], v94 offset0:24 offset1:28
	s_waitcnt lgkmcnt(0)
	v_cvt_pk_bf16_f32 v105, v106, v107
	v_lshl_add_u64 v[108:109], v[108:109], 1, s[36:37]
	v_ashrrev_i32_e32 v110, 31, v101
	ds_read2st64_b32 v[106:107], v95 offset1:4
	global_store_dwordx4 v[108:109], v[102:105], off
	v_mad_u64_u32 v[108:109], s[24:25], s30, v101, v[8:9]
	s_waitcnt lgkmcnt(0)
	v_cvt_pk_bf16_f32 v102, v106, v107
	ds_read2st64_b32 v[104:105], v95 offset0:8 offset1:12
	v_mul_lo_u32 v101, s31, v101
	v_mul_lo_u32 v110, s30, v110
	s_waitcnt lgkmcnt(0)
	v_cvt_pk_bf16_f32 v103, v104, v105
	ds_read2st64_b32 v[104:105], v95 offset0:16 offset1:20
	v_add3_u32 v109, v101, v109, v110
	s_waitcnt lgkmcnt(0)
	v_cvt_pk_bf16_f32 v104, v104, v105
	ds_read2st64_b32 v[106:107], v95 offset0:24 offset1:28
	s_waitcnt lgkmcnt(0)
	v_cvt_pk_bf16_f32 v105, v106, v107
	v_lshl_add_u64 v[108:109], v[108:109], 1, s[36:37]
	ds_read2st64_b32 v[106:107], v96 offset1:4
	global_store_dwordx4 v[108:109], v[102:105], off
	v_add_u32_e32 v101, s21, v80
	v_ashrrev_i32_e32 v108, 31, v101
	s_waitcnt lgkmcnt(0)
	v_cvt_pk_bf16_f32 v102, v106, v107
	ds_read2st64_b32 v[104:105], v96 offset0:8 offset1:12
	s_waitcnt lgkmcnt(0)
	v_cvt_pk_bf16_f32 v103, v104, v105
	ds_read2st64_b32 v[104:105], v96 offset0:16 offset1:20
	v_mad_u64_u32 v[8:9], s[24:25], s30, v101, v[8:9]
	s_waitcnt lgkmcnt(0)
	v_cvt_pk_bf16_f32 v104, v104, v105
	v_mul_lo_u32 v101, s31, v101
	v_mul_lo_u32 v105, s30, v108
	v_add3_u32 v9, v101, v9, v105
	v_lshl_add_u64 v[8:9], v[8:9], 1, s[36:37]
	ds_read2st64_b32 v[106:107], v96 offset0:24 offset1:28
	s_waitcnt lgkmcnt(0)
	v_cvt_pk_bf16_f32 v105, v106, v107
	global_store_dwordx4 v[8:9], v[102:105], off
	s_mov_b64 s[40:41], 0

; #define GAS __attribute__((address_space(1)))
; __device__ __forceinline__ void conv8_load(const ConvJob& J, int tid, f32x4 (&v)[16]) {
;     const int nblk = J.ncols / 256, k0 = 128 * (J.item / nblk), n0 = J.ncol0 + 256 * (J.item % nblk);
;     const int lane = tid & 63, w = tid >> 6, kg = lane & 7, nq = lane >> 3;
;     const GAS float* p = J.W + (size_t)(k0 + 16 * kg) * J.N + n0 + 32 * w + 4 * nq;
; #pragma unroll
;     for (int j = 0; j < 16; ++j) v[j] = *(const GAS f32x4*)(p + (size_t)j * J.N);
; }
;     ...
;         int q = q_lo + F.bid;
;         if (q < q_hi) {
;             f32x4 va[16], vb[16];
;             conv8_load(decode(q < I_IN ? q : q + NB16), tid, va);
.LBB0_400:
	v_cvt_f32_u32_e32 v3, s0
	s_sub_i32 s50, 0, s0
	s_abs_i32 s33, s1
	s_ashr_i32 s25, s1, 31
	v_rcp_iflag_f32_e32 v3, v3
	v_lshlrev_b32_e32 v4, 4, v2
	v_and_b32_e32 v130, 0x70, v4
	v_mov_b32_e32 v131, v163
	v_mul_f32_e32 v3, 0x4f7ffffe, v3
	v_cvt_u32_f32_e32 v3, v3
	s_nop 0
	v_readfirstlane_b32 s51, v3
	s_mul_i32 s50, s50, s51
	s_mul_hi_u32 s50, s51, s50
	s_add_i32 s51, s51, s50
	s_mul_hi_u32 s50, s33, s51
	s_mul_i32 s51, s50, s0
	s_sub_i32 s33, s33, s51
	s_add_i32 s58, s50, 1
	s_sub_i32 s51, s33, s0
	s_cmp_ge_u32 s33, s0
	s_cselect_b32 s50, s58, s50
	s_cselect_b32 s33, s51, s33
	s_add_i32 s51, s50, 1
	s_cmp_ge_u32 s33, s0
	s_cselect_b32 s33, s51, s50
	s_xor_b32 s33, s33, s25
	s_sub_i32 s25, s33, s25
	s_lshl_b32 s33, s25, 7
	s_mul_i32 s25, s25, s0
	s_sub_i32 s0, s1, s25
	v_or_b32_e32 v3, s33, v130
	s_lshl_b32 s0, s0, 8
	s_ashr_i32 s1, s33, 31
	s_add_i32 s0, s0, s24
	s_mul_i32 s1, s78, s1
	v_mul_lo_u32 v6, s79, v3
	v_mad_u64_u32 v[4:5], s[24:25], s78, v3, 0
	v_add3_u32 v5, v5, s1, v6
	v_ashrrev_i32_e32 v3, 1, v2
	v_lshl_add_u64 v[4:5], v[4:5], 2, s[80:81]
	s_ashr_i32 s1, s0, 31
	v_and_b32_e32 v132, 0xffffffe0, v3
	v_lshrrev_b32_e32 v2, 1, v2
	v_lshl_add_u64 v[4:5], s[0:1], 2, v[4:5]
	v_ashrrev_i32_e32 v133, 31, v132
	v_and_b32_e32 v134, 28, v2
	v_lshl_add_u64 v[4:5], v[132:133], 2, v[4:5]
	v_lshlrev_b32_e32 v162, 2, v134
	v_lshl_add_u64 v[2:3], v[4:5], 0, v[162:163]
	s_lshl_b64 s[0:1], s[78:79], 2
	v_lshl_add_u64 v[10:11], v[2:3], 0, s[0:1]
	global_load_dwordx4 v[2:5], v[2:3], off nt
	s_nop 0
	global_load_dwordx4 v[6:9], v[10:11], off nt
	v_lshl_add_u64 v[10:11], v[10:11], 0, s[0:1]
	v_lshl_add_u64 v[18:19], v[10:11], 0, s[0:1]
	global_load_dwordx4 v[10:13], v[10:11], off nt
	s_nop 0
	global_load_dwordx4 v[14:17], v[18:19], off nt
	v_lshl_add_u64 v[18:19], v[18:19], 0, s[0:1]
	v_lshl_add_u64 v[26:27], v[18:19], 0, s[0:1]
	v_lshl_add_u64 v[30:31], v[26:27], 0, s[0:1]
	v_lshl_add_u64 v[34:35], v[30:31], 0, s[0:1]
	v_lshl_add_u64 v[38:39], v[34:35], 0, s[0:1]
	v_lshl_add_u64 v[42:43], v[38:39], 0, s[0:1]
	v_lshl_add_u64 v[46:47], v[42:43], 0, s[0:1]
	global_load_dwordx4 v[18:21], v[18:19], off nt
	s_nop 0
	global_load_dwordx4 v[22:25], v[26:27], off nt
	v_or_b32_e32 v135, v134, v132
	global_load_dwordx4 v[26:29], v[30:31], off nt
	s_nop 0
	global_load_dwordx4 v[30:33], v[34:35], off nt
	s_nop 0
	global_load_dwordx4 v[34:37], v[38:39], off nt
	s_nop 0
	global_load_dwordx4 v[38:41], v[42:43], off nt
	s_nop 0
	global_load_dwordx4 v[42:45], v[46:47], off nt
	v_lshl_add_u64 v[46:47], v[46:47], 0, s[0:1]
	global_load_dwordx4 v[54:57], v[46:47], off nt
	v_lshl_add_u64 v[46:47], v[46:47], 0, s[0:1]
	global_load_dwordx4 v[62:65], v[46:47], off nt
	v_lshl_add_u64 v[46:47], v[46:47], 0, s[0:1]
	global_load_dwordx4 v[70:73], v[46:47], off nt
	v_lshl_add_u64 v[46:47], v[46:47], 0, s[0:1]
	global_load_dwordx4 v[78:81], v[46:47], off nt
	v_lshl_add_u64 v[46:47], v[46:47], 0, s[0:1]
	global_load_dwordx4 v[90:93], v[46:47], off nt
	s_movk_i32 s0, 0x7c
	v_bitop3_b32 v136, v134, s0, v132 bitop3:0xc8
	v_lshlrev_b32_e32 v46, 1, v136
	v_add_u32_e32 v47, 0xffffff81, v46
	v_cmp_gt_u32_e32 vcc, 64, v136
	v_or_b32_e32 v138, 0x80, v136
	s_mov_b32 s1, s66
	v_cndmask_b32_e32 v137, v47, v46, vcc
	s_branch .LBB0_404

; #define GAS __attribute__((address_space(1)))
; __device__ __forceinline__ void conv8_load(const ConvJob& J, int tid, f32x4 (&v)[16]) {
;     const int nblk = J.ncols / 256, k0 = 128 * (J.item / nblk), n0 = J.ncol0 + 256 * (J.item % nblk);
;     const int lane = tid & 63, w = tid >> 6, kg = lane & 7, nq = lane >> 3;
;     const GAS float* p = J.W + (size_t)(k0 + 16 * kg) * J.N + n0 + 32 * w + 4 * nq;
; #pragma unroll
;     for (int j = 0; j < 16; ++j) v[j] = *(const GAS f32x4*)(p + (size_t)j * J.N);
; }
;     ...
;                 const int q1 = q + F.G; const bool m1 = q1 < q_hi;
;                 if (m1) conv8_load(decode(q1 < I_IN ? q1 : q1 + NB16), tid, vb);
.LBB0_431:
	v_cvt_f32_u32_e32 v46, s25
	s_sub_i32 s58, 0, s25
	s_abs_i32 s51, s24
	s_ashr_i32 s33, s24, 31
	v_rcp_iflag_f32_e32 v46, v46
	v_lshlrev_b32_e32 v162, 2, v134
	v_mul_f32_e32 v46, 0x4f7ffffe, v46
	v_cvt_u32_f32_e32 v46, v46
	s_nop 0
	v_readfirstlane_b32 s59, v46
	s_mul_i32 s58, s58, s59
	s_mul_hi_u32 s58, s59, s58
	s_add_i32 s59, s59, s58
	s_mul_hi_u32 s58, s51, s59
	s_mul_i32 s59, s58, s25
	s_sub_i32 s51, s51, s59
	s_add_i32 s60, s58, 1
	s_sub_i32 s59, s51, s25
	s_cmp_ge_u32 s51, s25
	s_cselect_b32 s58, s60, s58
	s_cselect_b32 s51, s59, s51
	s_add_i32 s59, s58, 1
	s_cmp_ge_u32 s51, s25
	s_cselect_b32 s51, s59, s58
	s_xor_b32 s51, s51, s33
	s_sub_i32 s33, s51, s33
	s_lshl_b32 s51, s33, 7
	s_mul_i32 s33, s33, s25
	s_sub_i32 s24, s24, s33
	v_or_b32_e32 v46, s51, v130
	s_ashr_i32 s25, s51, 31
	s_lshl_b32 s24, s24, 8
	s_mul_i32 s25, s82, s25
	s_add_i32 s24, s24, s50
	v_mul_lo_u32 v48, s83, v46
	v_mad_u64_u32 v[46:47], s[50:51], s82, v46, 0
	v_add3_u32 v47, v47, s25, v48
	v_lshl_add_u64 v[46:47], v[46:47], 2, s[80:81]
	s_ashr_i32 s25, s24, 31
	v_lshl_add_u64 v[46:47], s[24:25], 2, v[46:47]
	v_lshl_add_u64 v[46:47], v[132:133], 2, v[46:47]
	v_lshl_add_u64 v[46:47], v[46:47], 0, v[162:163]
	s_lshl_b64 s[24:25], s[82:83], 2
	v_lshl_add_u64 v[58:59], v[46:47], 0, s[24:25]
	global_load_dwordx4 v[46:49], v[46:47], off nt
	s_nop 0
	global_load_dwordx4 v[50:53], v[58:59], off nt
	v_lshl_add_u64 v[58:59], v[58:59], 0, s[24:25]
	v_lshl_add_u64 v[74:75], v[58:59], 0, s[24:25]
	global_load_dwordx4 v[58:61], v[58:59], off nt
	s_nop 0
	global_load_dwordx4 v[66:69], v[74:75], off nt
	v_lshl_add_u64 v[74:75], v[74:75], 0, s[24:25]
	v_lshl_add_u64 v[86:87], v[74:75], 0, s[24:25]
	v_lshl_add_u64 v[94:95], v[86:87], 0, s[24:25]
	v_lshl_add_u64 v[98:99], v[94:95], 0, s[24:25]
	v_lshl_add_u64 v[102:103], v[98:99], 0, s[24:25]
	v_lshl_add_u64 v[106:107], v[102:103], 0, s[24:25]
	v_lshl_add_u64 v[110:111], v[106:107], 0, s[24:25]
	v_lshl_add_u64 v[114:115], v[110:111], 0, s[24:25]
	v_lshl_add_u64 v[118:119], v[114:115], 0, s[24:25]
	v_lshl_add_u64 v[122:123], v[118:119], 0, s[24:25]
	v_lshl_add_u64 v[126:127], v[122:123], 0, s[24:25]
	global_load_dwordx4 v[74:77], v[74:75], off nt
	s_nop 0
	global_load_dwordx4 v[82:85], v[86:87], off nt
	s_nop 0
	global_load_dwordx4 v[86:89], v[94:95], off nt
	s_nop 0
	global_load_dwordx4 v[94:97], v[98:99], off nt
	s_nop 0
	global_load_dwordx4 v[98:101], v[102:103], off nt
	s_nop 0
	global_load_dwordx4 v[102:105], v[106:107], off nt
	s_nop 0
	global_load_dwordx4 v[106:109], v[110:111], off nt
	s_nop 0
	global_load_dwordx4 v[110:113], v[114:115], off nt
	s_nop 0
	global_load_dwordx4 v[114:117], v[118:119], off nt
	s_nop 0
	global_load_dwordx4 v[118:121], v[122:123], off nt
	s_nop 0
	global_load_dwordx4 v[122:125], v[126:127], off nt
	v_lshl_add_u64 v[126:127], v[126:127], 0, s[24:25]
	global_load_dwordx4 v[126:129], v[126:127], off nt

; #define GAS __attribute__((address_space(1)))
; __device__ __forceinline__ void conv8_load(const ConvJob& J, int tid, f32x4 (&v)[16]) {
;     const int nblk = J.ncols / 256, k0 = 128 * (J.item / nblk), n0 = J.ncol0 + 256 * (J.item % nblk);
;     const int lane = tid & 63, w = tid >> 6, kg = lane & 7, nq = lane >> 3;
;     const GAS float* p = J.W + (size_t)(k0 + 16 * kg) * J.N + n0 + 32 * w + 4 * nq;
; #pragma unroll
;     for (int j = 0; j < 16; ++j) v[j] = *(const GAS f32x4*)(p + (size_t)j * J.N);
; }
;     ...
;             for (;;) {
;                 const int q1 = q + F.G; const bool m1 = q1 < q_hi;
;                 if (m1) conv8_load(decode(q1 < I_IN ? q1 : q1 + NB16), tid, vb);
;                 conv8_store(decode(q < I_IN ? q : q + NB16), tid, va);
;                 if (!m1) break;
;                 const int q2 = q1 + F.G; const bool m2 = q2 < q_hi;
;                 if (m2) conv8_load(decode(q2 < I_IN ? q2 : q2 + NB16), tid, va);
;                 conv8_store(decode(q1 < I_IN ? q1 : q1 + NB16), tid, vb);
;                 if (!m2) break;
;                 q = q2; }
.LBB0_527:
	v_cvt_f32_u32_e32 v2, s24
	s_sub_i32 s51, 0, s24
	s_abs_i32 s50, s1
	s_ashr_i32 s25, s1, 31
	v_rcp_iflag_f32_e32 v2, v2
	v_lshlrev_b32_e32 v162, 2, v134
	v_mul_f32_e32 v2, 0x4f7ffffe, v2
	v_cvt_u32_f32_e32 v2, v2
	s_nop 0
	v_readfirstlane_b32 s58, v2
	s_mul_i32 s51, s51, s58
	s_mul_hi_u32 s51, s58, s51
	s_add_i32 s58, s58, s51
	s_mul_hi_u32 s51, s50, s58
	s_mul_i32 s58, s51, s24
	s_sub_i32 s50, s50, s58
	s_add_i32 s59, s51, 1
	s_sub_i32 s58, s50, s24
	s_cmp_ge_u32 s50, s24
	s_cselect_b32 s51, s59, s51
	s_cselect_b32 s50, s58, s50
	s_add_i32 s58, s51, 1
	s_cmp_ge_u32 s50, s24
	s_cselect_b32 s50, s58, s51
	s_xor_b32 s50, s50, s25
	s_sub_i32 s25, s50, s25
	s_lshl_b32 s50, s25, 7
	s_mul_i32 s25, s25, s24
	s_sub_i32 s1, s1, s25
	v_or_b32_e32 v2, s50, v130
	s_ashr_i32 s24, s50, 31
	s_lshl_b32 s1, s1, 8
	s_mul_i32 s25, s80, s24
	v_mul_lo_u32 v4, s81, v2
	v_mad_u64_u32 v[2:3], s[50:51], s80, v2, 0
	s_add_i32 s24, s1, s33
	v_add3_u32 v3, v3, s25, v4
	v_lshl_add_u64 v[2:3], v[2:3], 2, s[78:79]
	s_ashr_i32 s25, s24, 31
	v_lshl_add_u64 v[2:3], s[24:25], 2, v[2:3]
	v_lshl_add_u64 v[2:3], v[132:133], 2, v[2:3]
	v_lshl_add_u64 v[2:3], v[2:3], 0, v[162:163]
	s_lshl_b64 s[24:25], s[80:81], 2
	v_lshl_add_u64 v[10:11], v[2:3], 0, s[24:25]
	global_load_dwordx4 v[2:5], v[2:3], off nt
	s_nop 0
	global_load_dwordx4 v[6:9], v[10:11], off nt
	v_lshl_add_u64 v[10:11], v[10:11], 0, s[24:25]
	v_lshl_add_u64 v[18:19], v[10:11], 0, s[24:25]
	global_load_dwordx4 v[10:13], v[10:11], off nt
	s_nop 0
	global_load_dwordx4 v[14:17], v[18:19], off nt
	v_lshl_add_u64 v[18:19], v[18:19], 0, s[24:25]
	v_lshl_add_u64 v[26:27], v[18:19], 0, s[24:25]
	v_lshl_add_u64 v[30:31], v[26:27], 0, s[24:25]
	v_lshl_add_u64 v[34:35], v[30:31], 0, s[24:25]
	v_lshl_add_u64 v[38:39], v[34:35], 0, s[24:25]
	v_lshl_add_u64 v[42:43], v[38:39], 0, s[24:25]
	v_lshl_add_u64 v[54:55], v[42:43], 0, s[24:25]
	v_lshl_add_u64 v[62:63], v[54:55], 0, s[24:25]
	v_lshl_add_u64 v[70:71], v[62:63], 0, s[24:25]
	v_lshl_add_u64 v[78:79], v[70:71], 0, s[24:25]
	v_lshl_add_u64 v[90:91], v[78:79], 0, s[24:25]
	global_load_dwordx4 v[18:21], v[18:19], off nt
	s_nop 0
	global_load_dwordx4 v[22:25], v[26:27], off nt
	s_nop 0
	global_load_dwordx4 v[26:29], v[30:31], off nt
	s_nop 0
	global_load_dwordx4 v[30:33], v[34:35], off nt
	s_nop 0
	global_load_dwordx4 v[34:37], v[38:39], off nt
	s_nop 0
	global_load_dwordx4 v[38:41], v[42:43], off nt
	s_nop 0
	global_load_dwordx4 v[42:45], v[54:55], off nt
	s_nop 0
	global_load_dwordx4 v[54:57], v[62:63], off nt
	s_nop 0
	global_load_dwordx4 v[62:65], v[70:71], off nt
	s_nop 0
	global_load_dwordx4 v[70:73], v[78:79], off nt
	s_nop 0
	global_load_dwordx4 v[78:81], v[90:91], off nt
	v_lshl_add_u64 v[90:91], v[90:91], 0, s[24:25]
	global_load_dwordx4 v[90:93], v[90:91], off nt

; #define GAS __attribute__((address_space(1)))
; #define LDS_BARRIER() asm volatile("s_waitcnt lgkmcnt(0)\n\ts_barrier" ::: "memory")
; __device__ __forceinline__ void conv8_load(const ConvJob& J, int tid, f32x4 (&v)[16]) {
;     const int nblk = J.ncols / 256, k0 = 128 * (J.item / nblk), n0 = J.ncol0 + 256 * (J.item % nblk);
;     const int lane = tid & 63, w = tid >> 6, kg = lane & 7, nq = lane >> 3;
;     const GAS float* p = J.W + (size_t)(k0 + 16 * kg) * J.N + n0 + 32 * w + 4 * nq;
; #pragma unroll
;     for (int j = 0; j < 16; ++j) v[j] = *(const GAS f32x4*)(p + (size_t)j * J.N);
; }
;     ...
;             for (;;) {
;                 if (tid == 0) *qw = __hip_atomic_fetch_add(ctr, 1u, RLX_AGENT);
;                 LDS_BARRIER();
;                 const int qd = q_hi + __builtin_amdgcn_readfirstlane((int)*qw);
;                 LDS_BARRIER();
;                 if (qd >= q_end) break;
;                 const ConvJob j = decode(qd < I_IN ? qd : qd + NB16); f32x4 v[16]; conv8_load(j, tid, v); conv8_store(j, tid, v); }
.LBB0_631:
	v_cvt_f32_u32_e32 v2, s50
	s_sub_i32 s56, 0, s50
	s_abs_i32 s51, s33
	s_ashr_i32 s34, s33, 31
	v_rcp_iflag_f32_e32 v2, v2
	s_nop 0
	v_mul_f32_e32 v2, 0x4f7ffffe, v2
	v_cvt_u32_f32_e32 v2, v2
	s_nop 0
	v_readfirstlane_b32 s57, v2
	s_mul_i32 s56, s56, s57
	s_mul_hi_u32 s56, s57, s56
	s_add_i32 s57, s57, s56
	s_mul_hi_u32 s56, s51, s57
	s_mul_i32 s57, s56, s50
	s_sub_i32 s51, s51, s57
	s_add_i32 s58, s56, 1
	s_sub_i32 s57, s51, s50
	s_cmp_ge_u32 s51, s50
	s_cselect_b32 s56, s58, s56
	s_cselect_b32 s51, s57, s51
	s_add_i32 s57, s56, 1
	s_cmp_ge_u32 s51, s50
	s_cselect_b32 s51, s57, s56
	s_xor_b32 s51, s51, s34
	s_sub_i32 s34, s51, s34
	s_lshl_b32 s58, s34, 7
	s_mul_i32 s34, s34, s50
	s_sub_i32 s33, s33, s34
	v_or_b32_e32 v2, s58, v66
	s_ashr_i32 s59, s58, 31
	s_lshl_b32 s33, s33, 8
	s_mul_i32 s34, s62, s59
	v_mul_lo_u32 v4, s63, v2
	v_mad_u64_u32 v[2:3], s[50:51], s62, v2, 0
	s_add_i32 s64, s33, s27
	v_add3_u32 v3, v3, s34, v4
	v_lshl_add_u64 v[2:3], v[2:3], 2, s[60:61]
	s_ashr_i32 s65, s64, 31
	v_lshl_add_u64 v[2:3], s[64:65], 2, v[2:3]
	v_lshl_add_u64 v[2:3], v[68:69], 2, v[2:3]
	v_lshl_add_u64 v[2:3], v[2:3], 0, v[70:71]
	s_lshl_b64 s[50:51], s[62:63], 2
	v_lshl_add_u64 v[4:5], v[2:3], 0, s[50:51]
	global_load_dwordx4 v[26:29], v[2:3], off nt
	global_load_dwordx4 v[30:33], v[4:5], off nt
	v_lshl_add_u64 v[2:3], v[4:5], 0, s[50:51]
	v_lshl_add_u64 v[4:5], v[2:3], 0, s[50:51]
	global_load_dwordx4 v[58:61], v[2:3], off nt
	global_load_dwordx4 v[62:65], v[4:5], off nt
	v_lshl_add_u64 v[2:3], v[4:5], 0, s[50:51]
	v_lshl_add_u64 v[4:5], v[2:3], 0, s[50:51]
	global_load_dwordx4 v[42:45], v[2:3], off nt
	global_load_dwordx4 v[46:49], v[4:5], off nt
	v_lshl_add_u64 v[2:3], v[4:5], 0, s[50:51]
	global_load_dwordx4 v[34:37], v[2:3], off nt
	v_lshl_add_u64 v[2:3], v[2:3], 0, s[50:51]
	global_load_dwordx4 v[38:41], v[2:3], off nt
	v_lshl_add_u64 v[2:3], v[2:3], 0, s[50:51]
	global_load_dwordx4 v[6:9], v[2:3], off nt
	v_lshl_add_u64 v[2:3], v[2:3], 0, s[50:51]
	global_load_dwordx4 v[18:21], v[2:3], off nt
	v_lshl_add_u64 v[2:3], v[2:3], 0, s[50:51]
	global_load_dwordx4 v[50:53], v[2:3], off nt
	v_lshl_add_u64 v[2:3], v[2:3], 0, s[50:51]
	global_load_dwordx4 v[54:57], v[2:3], off nt
	v_lshl_add_u64 v[2:3], v[2:3], 0, s[50:51]
	global_load_dwordx4 v[10:13], v[2:3], off nt
	v_lshl_add_u64 v[2:3], v[2:3], 0, s[50:51]
	v_lshl_add_u64 v[14:15], v[2:3], 0, s[50:51]
	global_load_dwordx4 v[22:25], v[2:3], off nt
	v_add_u32_e32 v76, s33, v1
	global_load_dwordx4 v[2:5], v[14:15], off nt
	v_lshl_add_u64 v[14:15], v[14:15], 0, s[50:51]
	global_load_dwordx4 v[14:17], v[14:15], off nt
	s_cmp_lt_i32 s25, 2
	s_mov_b64 s[60:61], -1
	s_cbranch_scc1 .LBB0_637
	s_cmp_gt_i32 s25, 2
	v_lshlrev_b32_e32 v78, 1, v76
	s_cbranch_scc0 .LBB0_634
	v_and_or_b32 v77, v78, s3, v74
	s_mov_b64 s[60:61], 0

; #define GAS __attribute__((address_space(1)))
; __device__ __forceinline__ void conv8_load(const ConvJob& J, int tid, f32x4 (&v)[16]) {
;     const int nblk = J.ncols / 256, k0 = 128 * (J.item / nblk), n0 = J.ncol0 + 256 * (J.item % nblk);
;     const int lane = tid & 63, w = tid >> 6, kg = lane & 7, nq = lane >> 3;
;     const GAS float* p = J.W + (size_t)(k0 + 16 * kg) * J.N + n0 + 32 * w + 4 * nq;
; #pragma unroll
;     for (int j = 0; j < 16; ++j) v[j] = *(const GAS f32x4*)(p + (size_t)j * J.N);
; }
;     ...
;         int q = q_lo + F.bid;
;         if (q < q_hi) {
;             f32x4 va[16], vb[16];
;             conv8_load(decode(q < I_IN ? q : q + NB16), tid, va);
.LBB0_1588:
	v_cvt_f32_u32_e32 v2, s12
	s_sub_i32 s44, 0, s12
	s_abs_i32 s39, s13
	s_ashr_i32 s2, s13, 31
	v_rcp_iflag_f32_e32 v2, v2
	v_lshlrev_b32_e32 v3, 4, v135
	v_and_b32_e32 v130, 0x70, v3
	v_mov_b32_e32 v131, v163
	v_mul_f32_e32 v2, 0x4f7ffffe, v2
	v_cvt_u32_f32_e32 v2, v2
	s_nop 0
	v_readfirstlane_b32 s45, v2
	s_mul_i32 s44, s44, s45
	s_mul_hi_u32 s44, s45, s44
	s_add_i32 s45, s45, s44
	s_mul_hi_u32 s44, s39, s45
	s_mul_i32 s45, s44, s12
	s_sub_i32 s39, s39, s45
	s_add_i32 s46, s44, 1
	s_sub_i32 s45, s39, s12
	s_cmp_ge_u32 s39, s12
	s_cselect_b32 s44, s46, s44
	s_cselect_b32 s39, s45, s39
	s_add_i32 s45, s44, 1
	s_cmp_ge_u32 s39, s12
	s_cselect_b32 s39, s45, s44
	s_xor_b32 s39, s39, s2
	s_sub_i32 s2, s39, s2
	s_lshl_b32 s39, s2, 7
	s_mul_i32 s2, s2, s12
	s_sub_i32 s2, s13, s2
	s_lshl_b32 s2, s2, 8
	v_or_b32_e32 v2, s39, v130
	s_add_i32 s12, s2, s38
	s_ashr_i32 s2, s39, 31
	s_mul_i32 s2, s74, s2
	v_mul_lo_u32 v4, s75, v2
	v_mad_u64_u32 v[2:3], s[38:39], s74, v2, 0
	v_add3_u32 v3, v3, s2, v4
	v_ashrrev_i32_e32 v4, 1, v135
	v_lshl_add_u64 v[2:3], v[2:3], 2, s[76:77]
	s_ashr_i32 s13, s12, 31
	v_and_b32_e32 v132, 0xffffffe0, v4
	v_lshrrev_b32_e32 v4, 1, v135
	v_lshl_add_u64 v[2:3], s[12:13], 2, v[2:3]
	v_ashrrev_i32_e32 v133, 31, v132
	v_and_b32_e32 v134, 28, v4
	v_lshl_add_u64 v[2:3], v[132:133], 2, v[2:3]
	v_lshlrev_b32_e32 v162, 2, v134
	v_lshl_add_u64 v[2:3], v[2:3], 0, v[162:163]
	s_lshl_b64 s[12:13], s[74:75], 2
	v_lshl_add_u64 v[10:11], v[2:3], 0, s[12:13]
	global_load_dwordx4 v[2:5], v[2:3], off nt
	s_nop 0
	global_load_dwordx4 v[6:9], v[10:11], off nt
	v_lshl_add_u64 v[10:11], v[10:11], 0, s[12:13]
	v_lshl_add_u64 v[18:19], v[10:11], 0, s[12:13]
	global_load_dwordx4 v[10:13], v[10:11], off nt
	s_nop 0
	global_load_dwordx4 v[14:17], v[18:19], off nt
	v_lshl_add_u64 v[18:19], v[18:19], 0, s[12:13]
	v_lshl_add_u64 v[26:27], v[18:19], 0, s[12:13]
	v_lshl_add_u64 v[30:31], v[26:27], 0, s[12:13]
	v_lshl_add_u64 v[34:35], v[30:31], 0, s[12:13]
	s_waitcnt vmcnt(0)
	v_lshl_add_u64 v[38:39], v[34:35], 0, s[12:13]
	v_lshl_add_u64 v[42:43], v[38:39], 0, s[12:13]
	v_lshl_add_u64 v[46:47], v[42:43], 0, s[12:13]
	global_load_dwordx4 v[18:21], v[18:19], off nt
	s_nop 0
	global_load_dwordx4 v[22:25], v[26:27], off nt
	s_movk_i32 s2, 0x7c
	global_load_dwordx4 v[26:29], v[30:31], off nt
	v_bitop3_b32 v137, v134, s2, v132 bitop3:0xc8
	global_load_dwordx4 v[30:33], v[34:35], off nt
	v_cmp_gt_u32_e32 vcc, 64, v137
	global_load_dwordx4 v[34:37], v[38:39], off nt
	v_or_b32_e32 v136, v134, v132
	global_load_dwordx4 v[38:41], v[42:43], off nt
	v_or_b32_e32 v139, 0x80, v137
	global_load_dwordx4 v[42:45], v[46:47], off nt
	v_lshl_add_u64 v[46:47], v[46:47], 0, s[12:13]
	global_load_dwordx4 v[54:57], v[46:47], off nt
	v_lshl_add_u64 v[46:47], v[46:47], 0, s[12:13]
	global_load_dwordx4 v[62:65], v[46:47], off nt
	v_lshl_add_u64 v[46:47], v[46:47], 0, s[12:13]
	global_load_dwordx4 v[70:73], v[46:47], off nt
	v_lshl_add_u64 v[46:47], v[46:47], 0, s[12:13]
	global_load_dwordx4 v[78:81], v[46:47], off nt
	v_lshl_add_u64 v[46:47], v[46:47], 0, s[12:13]
	global_load_dwordx4 v[90:93], v[46:47], off nt
	v_lshlrev_b32_e32 v46, 1, v137
	v_add_u32_e32 v47, 0xffffff81, v46
	v_cndmask_b32_e32 v138, v47, v46, vcc
	v_readlane_b32 s13, v254, 41
	s_branch .LBB0_1592

; #define GAS __attribute__((address_space(1)))
; __device__ __forceinline__ void conv8_load(const ConvJob& J, int tid, f32x4 (&v)[16]) {
;     const int nblk = J.ncols / 256, k0 = 128 * (J.item / nblk), n0 = J.ncol0 + 256 * (J.item % nblk);
;     const int lane = tid & 63, w = tid >> 6, kg = lane & 7, nq = lane >> 3;
;     const GAS float* p = J.W + (size_t)(k0 + 16 * kg) * J.N + n0 + 32 * w + 4 * nq;
; #pragma unroll
;     for (int j = 0; j < 16; ++j) v[j] = *(const GAS f32x4*)(p + (size_t)j * J.N);
; }
;     ...
;             for (;;) {
;                 const int q1 = q + F.G; const bool m1 = q1 < q_hi;
;                 if (m1) conv8_load(decode(q1 < I_IN ? q1 : q1 + NB16), tid, vb);
;                 conv8_store(decode(q < I_IN ? q : q + NB16), tid, va);
;                 if (!m1) break;
;                 const int q2 = q1 + F.G; const bool m2 = q2 < q_hi;
;                 if (m2) conv8_load(decode(q2 < I_IN ? q2 : q2 + NB16), tid, va);
;                 conv8_store(decode(q1 < I_IN ? q1 : q1 + NB16), tid, vb);
;                 if (!m2) break;
;                 q = q2; }
.LBB0_1619:
	v_cvt_f32_u32_e32 v46, s39
	s_sub_i32 s46, 0, s39
	s_abs_i32 s44, s38
	s_ashr_i32 s2, s38, 31
	v_rcp_iflag_f32_e32 v46, v46
	v_lshlrev_b32_e32 v162, 2, v134
	v_mul_f32_e32 v46, 0x4f7ffffe, v46
	v_cvt_u32_f32_e32 v46, v46
	s_nop 0
	v_readfirstlane_b32 s49, v46
	s_mul_i32 s46, s46, s49
	s_mul_hi_u32 s46, s49, s46
	s_add_i32 s49, s49, s46
	s_mul_hi_u32 s46, s44, s49
	s_mul_i32 s49, s46, s39
	s_sub_i32 s44, s44, s49
	s_add_i32 s50, s46, 1
	s_sub_i32 s49, s44, s39
	s_cmp_ge_u32 s44, s39
	s_cselect_b32 s46, s50, s46
	s_cselect_b32 s44, s49, s44
	s_add_i32 s49, s46, 1
	s_cmp_ge_u32 s44, s39
	s_cselect_b32 s44, s49, s46
	s_xor_b32 s44, s44, s2
	s_sub_i32 s2, s44, s2
	s_lshl_b32 s44, s2, 7
	s_mul_i32 s2, s2, s39
	s_sub_i32 s2, s38, s2
	v_or_b32_e32 v46, s44, v130
	s_ashr_i32 s38, s44, 31
	s_lshl_b32 s2, s2, 8
	s_mul_i32 s39, s78, s38
	s_add_i32 s38, s2, s45
	v_mul_lo_u32 v48, s79, v46
	v_mad_u64_u32 v[46:47], s[44:45], s78, v46, 0
	v_add3_u32 v47, v47, s39, v48
	v_lshl_add_u64 v[46:47], v[46:47], 2, s[76:77]
	s_ashr_i32 s39, s38, 31
	v_lshl_add_u64 v[46:47], s[38:39], 2, v[46:47]
	v_lshl_add_u64 v[46:47], v[132:133], 2, v[46:47]
	v_lshl_add_u64 v[46:47], v[46:47], 0, v[162:163]
	s_lshl_b64 s[38:39], s[78:79], 2
	v_lshl_add_u64 v[58:59], v[46:47], 0, s[38:39]
	global_load_dwordx4 v[46:49], v[46:47], off nt
	s_nop 0
	global_load_dwordx4 v[50:53], v[58:59], off nt
	v_lshl_add_u64 v[58:59], v[58:59], 0, s[38:39]
	v_lshl_add_u64 v[74:75], v[58:59], 0, s[38:39]
	global_load_dwordx4 v[58:61], v[58:59], off nt
	s_nop 0
	global_load_dwordx4 v[66:69], v[74:75], off nt
	v_lshl_add_u64 v[74:75], v[74:75], 0, s[38:39]
	v_lshl_add_u64 v[86:87], v[74:75], 0, s[38:39]
	v_lshl_add_u64 v[94:95], v[86:87], 0, s[38:39]
	v_lshl_add_u64 v[98:99], v[94:95], 0, s[38:39]
	v_lshl_add_u64 v[102:103], v[98:99], 0, s[38:39]
	v_lshl_add_u64 v[106:107], v[102:103], 0, s[38:39]
	v_lshl_add_u64 v[110:111], v[106:107], 0, s[38:39]
	v_lshl_add_u64 v[114:115], v[110:111], 0, s[38:39]
	v_lshl_add_u64 v[118:119], v[114:115], 0, s[38:39]
	v_lshl_add_u64 v[122:123], v[118:119], 0, s[38:39]
	v_lshl_add_u64 v[126:127], v[122:123], 0, s[38:39]
	global_load_dwordx4 v[74:77], v[74:75], off nt
	s_nop 0
	global_load_dwordx4 v[82:85], v[86:87], off nt
	s_nop 0
	global_load_dwordx4 v[86:89], v[94:95], off nt
	s_nop 0
	global_load_dwordx4 v[94:97], v[98:99], off nt
	s_nop 0
	global_load_dwordx4 v[98:101], v[102:103], off nt
	s_nop 0
	global_load_dwordx4 v[102:105], v[106:107], off nt
	s_nop 0
	global_load_dwordx4 v[106:109], v[110:111], off nt
	s_nop 0
	global_load_dwordx4 v[110:113], v[114:115], off nt
	s_nop 0
	global_load_dwordx4 v[114:117], v[118:119], off nt
	s_nop 0
	global_load_dwordx4 v[118:121], v[122:123], off nt
	s_nop 0
	global_load_dwordx4 v[122:125], v[126:127], off nt
	v_lshl_add_u64 v[126:127], v[126:127], 0, s[38:39]
	global_load_dwordx4 v[126:129], v[126:127], off nt

; #define GAS __attribute__((address_space(1)))
; __device__ __forceinline__ void conv8_load(const ConvJob& J, int tid, f32x4 (&v)[16]) {
;     const int nblk = J.ncols / 256, k0 = 128 * (J.item / nblk), n0 = J.ncol0 + 256 * (J.item % nblk);
;     const int lane = tid & 63, w = tid >> 6, kg = lane & 7, nq = lane >> 3;
;     const GAS float* p = J.W + (size_t)(k0 + 16 * kg) * J.N + n0 + 32 * w + 4 * nq;
; #pragma unroll
;     for (int j = 0; j < 16; ++j) v[j] = *(const GAS f32x4*)(p + (size_t)j * J.N);
; }
;     ...
;             for (;;) {
;                 const int q1 = q + F.G; const bool m1 = q1 < q_hi;
;                 if (m1) conv8_load(decode(q1 < I_IN ? q1 : q1 + NB16), tid, vb);
;                 conv8_store(decode(q < I_IN ? q : q + NB16), tid, va);
;                 if (!m1) break;
;                 const int q2 = q1 + F.G; const bool m2 = q2 < q_hi;
;                 if (m2) conv8_load(decode(q2 < I_IN ? q2 : q2 + NB16), tid, va);
;                 conv8_store(decode(q1 < I_IN ? q1 : q1 + NB16), tid, vb);
;                 if (!m2) break;
;                 q = q2; }
.LBB0_1714:
	v_cvt_f32_u32_e32 v2, s38
	s_sub_i32 s45, 0, s38
	s_abs_i32 s39, s13
	s_ashr_i32 s2, s13, 31
	v_rcp_iflag_f32_e32 v2, v2
	v_lshlrev_b32_e32 v162, 2, v134
	v_mul_f32_e32 v2, 0x4f7ffffe, v2
	v_cvt_u32_f32_e32 v2, v2
	s_nop 0
	v_readfirstlane_b32 s46, v2
	s_mul_i32 s45, s45, s46
	s_mul_hi_u32 s45, s46, s45
	s_add_i32 s46, s46, s45
	s_mul_hi_u32 s45, s39, s46
	s_mul_i32 s46, s45, s38
	s_sub_i32 s39, s39, s46
	s_add_i32 s49, s45, 1
	s_sub_i32 s46, s39, s38
	s_cmp_ge_u32 s39, s38
	s_cselect_b32 s45, s49, s45
	s_cselect_b32 s39, s46, s39
	s_add_i32 s46, s45, 1
	s_cmp_ge_u32 s39, s38
	s_cselect_b32 s39, s46, s45
	s_xor_b32 s39, s39, s2
	s_sub_i32 s2, s39, s2
	s_lshl_b32 s39, s2, 7
	s_mul_i32 s2, s2, s38
	s_sub_i32 s2, s13, s2
	v_or_b32_e32 v2, s39, v130
	s_ashr_i32 s13, s39, 31
	s_lshl_b32 s2, s2, 8
	s_mul_i32 s13, s76, s13
	s_add_i32 s38, s2, s44
	v_mul_lo_u32 v4, s77, v2
	v_mad_u64_u32 v[2:3], s[44:45], s76, v2, 0
	v_add3_u32 v3, v3, s13, v4
	v_lshl_add_u64 v[2:3], v[2:3], 2, s[74:75]
	s_ashr_i32 s39, s38, 31
	v_lshl_add_u64 v[2:3], s[38:39], 2, v[2:3]
	v_lshl_add_u64 v[2:3], v[132:133], 2, v[2:3]
	v_lshl_add_u64 v[2:3], v[2:3], 0, v[162:163]
	s_lshl_b64 s[38:39], s[76:77], 2
	v_lshl_add_u64 v[10:11], v[2:3], 0, s[38:39]
	global_load_dwordx4 v[2:5], v[2:3], off nt
	s_nop 0
	global_load_dwordx4 v[6:9], v[10:11], off nt
	v_lshl_add_u64 v[10:11], v[10:11], 0, s[38:39]
	v_lshl_add_u64 v[18:19], v[10:11], 0, s[38:39]
	global_load_dwordx4 v[10:13], v[10:11], off nt
	s_nop 0
	global_load_dwordx4 v[14:17], v[18:19], off nt
	v_lshl_add_u64 v[18:19], v[18:19], 0, s[38:39]
	v_lshl_add_u64 v[26:27], v[18:19], 0, s[38:39]
	v_lshl_add_u64 v[30:31], v[26:27], 0, s[38:39]
	v_lshl_add_u64 v[34:35], v[30:31], 0, s[38:39]
	v_lshl_add_u64 v[38:39], v[34:35], 0, s[38:39]
	v_lshl_add_u64 v[42:43], v[38:39], 0, s[38:39]
	v_lshl_add_u64 v[54:55], v[42:43], 0, s[38:39]
	v_lshl_add_u64 v[62:63], v[54:55], 0, s[38:39]
	v_lshl_add_u64 v[70:71], v[62:63], 0, s[38:39]
	v_lshl_add_u64 v[78:79], v[70:71], 0, s[38:39]
	v_lshl_add_u64 v[90:91], v[78:79], 0, s[38:39]
	global_load_dwordx4 v[18:21], v[18:19], off nt
	s_nop 0
	global_load_dwordx4 v[22:25], v[26:27], off nt
	s_nop 0
	global_load_dwordx4 v[26:29], v[30:31], off nt
	s_nop 0
	global_load_dwordx4 v[30:33], v[34:35], off nt
	s_nop 0
	global_load_dwordx4 v[34:37], v[38:39], off nt
	s_nop 0
	global_load_dwordx4 v[38:41], v[42:43], off nt
	s_nop 0
	global_load_dwordx4 v[42:45], v[54:55], off nt
	s_nop 0
	global_load_dwordx4 v[54:57], v[62:63], off nt
	s_nop 0
	global_load_dwordx4 v[62:65], v[70:71], off nt
	s_nop 0
	global_load_dwordx4 v[70:73], v[78:79], off nt
	s_nop 0
	global_load_dwordx4 v[78:81], v[90:91], off nt
	v_lshl_add_u64 v[90:91], v[90:91], 0, s[38:39]
	global_load_dwordx4 v[90:93], v[90:91], off nt

; #define GAS __attribute__((address_space(1)))
; #define LAS __attribute__((address_space(3)))
; __device__ __forceinline__ void conv_load(const ConvJob& J, int tid, f32x4 (&v)[16]) {
;     const int nblk = J.ncols / 256, k0 = 128 * (J.item / nblk), n0 = J.ncol0 + 256 * (J.item % nblk);
;     {
; #pragma unroll
;         for (int ii = 0; ii < 16; ++ii) { const int idx = tid + 512 * ii, k = idx >> 6, c4 = idx & 63; v[ii] = *(const GAS f32x4*)(J.W + (size_t)(k0 + k) * J.N + n0 + 4 * c4); }
;     }
; }
; __device__ __forceinline__ void conv_to_lds(const ConvJob& J, int tid, const f32x4 (&v)[16], LAS float* T) {
; #pragma unroll
;     for (int ii = 0; ii < 16; ++ii) { const int idx = tid + 512 * ii, k = idx >> 6, c4 = idx & 63; const int g = J.f8 ? ((k >> 4) & 7) : ((k >> 3) & 15);
;         *(LAS f32x4*)(T + k * 256 + 4 * (c4 ^ g)) = v[ii]; }
; }
.LBB0_1797:
	v_cvt_f32_ubyte0_e32 v114, s12
	v_rcp_iflag_f32_e32 v114, v114
	s_sub_i32 s24, 0, s12
	s_abs_i32 s13, s10
	s_ashr_i32 s2, s10, 31
	v_mul_f32_e32 v114, 0x4f7ffffe, v114
	v_cvt_u32_f32_e32 v114, v114
	v_xor_b32_e32 v113, v113, v23
	v_xor_b32_e32 v112, v112, v23
	v_xor_b32_e32 v111, v111, v23
	v_readfirstlane_b32 s25, v114
	s_mul_i32 s24, s24, s25
	s_mul_hi_u32 s24, s25, s24
	s_add_i32 s25, s25, s24
	s_mul_hi_u32 s24, s13, s25
	s_mul_i32 s25, s24, s12
	s_sub_i32 s13, s13, s25
	s_add_i32 s33, s24, 1
	s_sub_i32 s25, s13, s12
	s_cmp_ge_u32 s13, s12
	s_cselect_b32 s24, s33, s24
	s_cselect_b32 s13, s25, s13
	s_add_i32 s25, s24, 1
	s_cmp_ge_u32 s13, s12
	s_cselect_b32 s13, s25, s24
	s_xor_b32 s13, s13, s2
	s_sub_i32 s2, s13, s2
	s_lshl_b32 s74, s2, 7
	s_mul_i32 s2, s2, s12
	s_sub_i32 s2, s10, s2
	s_lshl_b32 s10, s2, 8
	s_add_i32 s12, s10, s11
	s_ashr_i32 s13, s12, 31
	v_add_u32_e32 v114, s74, v3
	v_add_u32_e32 v116, s74, v8
	v_add_u32_e32 v122, s74, v9
	v_add_u32_e32 v124, s74, v10
	v_add_u32_e32 v130, s74, v11
	v_add_u32_e32 v132, s74, v12
	v_add_u32_e32 v138, s74, v13
	v_add_u32_e32 v140, s74, v14
	v_add_u32_e32 v146, s74, v15
	v_add_u32_e32 v148, s74, v16
	v_add_u32_e32 v154, s74, v17
	v_add_u32_e32 v156, s74, v18
	v_add_u32_e32 v164, s74, v19
	v_add_u32_e32 v166, s74, v20
	v_add_u32_e32 v172, s74, v21
	v_add_u32_e32 v176, s74, v22
	v_mad_i64_i32 v[114:115], s[24:25], s82, v114, 0
	s_lshl_b64 s[84:85], s[12:13], 2
	v_mad_i64_i32 v[116:117], s[12:13], s82, v116, 0
	v_mad_i64_i32 v[122:123], s[12:13], s82, v122, 0
	v_mad_i64_i32 v[124:125], s[12:13], s82, v124, 0
	v_mad_i64_i32 v[130:131], s[12:13], s82, v130, 0
	v_mad_i64_i32 v[132:133], s[12:13], s82, v132, 0
	v_mad_i64_i32 v[138:139], s[12:13], s82, v138, 0
	v_mad_i64_i32 v[140:141], s[12:13], s82, v140, 0
	v_mad_i64_i32 v[146:147], s[12:13], s82, v146, 0
	v_mad_i64_i32 v[148:149], s[12:13], s82, v148, 0
	v_mad_i64_i32 v[154:155], s[12:13], s82, v154, 0
	v_mad_i64_i32 v[156:157], s[12:13], s82, v156, 0
	v_mad_i64_i32 v[164:165], s[12:13], s82, v164, 0
	v_mad_i64_i32 v[166:167], s[12:13], s82, v166, 0
	v_mad_i64_i32 v[172:173], s[12:13], s82, v172, 0
	v_mad_i64_i32 v[176:177], s[12:13], s82, v176, 0
	v_lshl_add_u64 v[114:115], v[114:115], 2, s[80:81]
	v_lshl_add_u64 v[116:117], v[116:117], 2, s[80:81]
	v_lshl_add_u64 v[122:123], v[122:123], 2, s[80:81]
	v_lshl_add_u64 v[124:125], v[124:125], 2, s[80:81]
	v_lshl_add_u64 v[130:131], v[130:131], 2, s[80:81]
	v_lshl_add_u64 v[132:133], v[132:133], 2, s[80:81]
	v_lshl_add_u64 v[138:139], v[138:139], 2, s[80:81]
	v_lshl_add_u64 v[140:141], v[140:141], 2, s[80:81]
	v_lshl_add_u64 v[146:147], v[146:147], 2, s[80:81]
	v_lshl_add_u64 v[148:149], v[148:149], 2, s[80:81]
	v_lshl_add_u64 v[154:155], v[154:155], 2, s[80:81]
	v_lshl_add_u64 v[156:157], v[156:157], 2, s[80:81]
	v_lshl_add_u64 v[164:165], v[164:165], 2, s[80:81]
	v_lshl_add_u64 v[166:167], v[166:167], 2, s[80:81]
	v_lshl_add_u64 v[172:173], v[172:173], 2, s[80:81]
	v_lshl_add_u64 v[176:177], v[176:177], 2, s[80:81]
	v_lshl_add_u64 v[114:115], v[114:115], 0, s[84:85]
	v_lshl_add_u64 v[116:117], v[116:117], 0, s[84:85]
	v_lshl_add_u64 v[122:123], v[122:123], 0, s[84:85]
	v_lshl_add_u64 v[124:125], v[124:125], 0, s[84:85]
	v_lshl_add_u64 v[130:131], v[130:131], 0, s[84:85]
	v_lshl_add_u64 v[132:133], v[132:133], 0, s[84:85]
	v_lshl_add_u64 v[138:139], v[138:139], 0, s[84:85]
	v_lshl_add_u64 v[140:141], v[140:141], 0, s[84:85]
	v_lshl_add_u64 v[146:147], v[146:147], 0, s[84:85]
	v_lshl_add_u64 v[148:149], v[148:149], 0, s[84:85]
	v_lshl_add_u64 v[154:155], v[154:155], 0, s[84:85]
	v_lshl_add_u64 v[156:157], v[156:157], 0, s[84:85]
	v_lshl_add_u64 v[164:165], v[164:165], 0, s[84:85]
	v_lshl_add_u64 v[166:167], v[166:167], 0, s[84:85]
	v_lshl_add_u64 v[172:173], v[172:173], 0, s[84:85]
	v_lshl_add_u64 v[176:177], v[176:177], 0, s[84:85]
	v_lshl_add_u64 v[114:115], v[114:115], 0, v[162:163]
	v_lshl_add_u64 v[118:119], v[116:117], 0, v[162:163]
	v_lshl_add_u64 v[122:123], v[122:123], 0, v[162:163]
	v_lshl_add_u64 v[126:127], v[124:125], 0, v[162:163]
	v_lshl_add_u64 v[130:131], v[130:131], 0, v[162:163]
	v_lshl_add_u64 v[134:135], v[132:133], 0, v[162:163]
	v_lshl_add_u64 v[138:139], v[138:139], 0, v[162:163]
	v_lshl_add_u64 v[142:143], v[140:141], 0, v[162:163]
	v_lshl_add_u64 v[146:147], v[146:147], 0, v[162:163]
	v_lshl_add_u64 v[150:151], v[148:149], 0, v[162:163]
	v_lshl_add_u64 v[154:155], v[154:155], 0, v[162:163]
	v_lshl_add_u64 v[158:159], v[156:157], 0, v[162:163]
	v_lshl_add_u64 v[164:165], v[164:165], 0, v[162:163]
	v_lshl_add_u64 v[168:169], v[166:167], 0, v[162:163]
	v_lshl_add_u64 v[172:173], v[172:173], 0, v[162:163]
	v_lshl_add_u64 v[176:177], v[176:177], 0, v[162:163]
	global_load_dwordx4 v[114:117], v[114:115], off nt
	s_nop 0
	global_load_dwordx4 v[118:121], v[118:119], off nt
	s_nop 0
	global_load_dwordx4 v[122:125], v[122:123], off nt
	s_nop 0
	global_load_dwordx4 v[126:129], v[126:127], off nt
	s_nop 0
	global_load_dwordx4 v[130:133], v[130:131], off nt
	s_nop 0
	global_load_dwordx4 v[134:137], v[134:135], off nt
	s_nop 0
	global_load_dwordx4 v[138:141], v[138:139], off nt
	s_nop 0
	global_load_dwordx4 v[142:145], v[142:143], off nt
	s_nop 0
	global_load_dwordx4 v[146:149], v[146:147], off nt
	s_nop 0
	global_load_dwordx4 v[150:153], v[150:151], off nt
	s_nop 0
	global_load_dwordx4 v[154:157], v[154:155], off nt
	s_nop 0
	global_load_dwordx4 v[158:161], v[158:159], off nt
	s_nop 0
	global_load_dwordx4 v[164:167], v[164:165], off nt
	s_nop 0
	global_load_dwordx4 v[168:171], v[168:169], off nt
	v_xor_b32_e32 v110, v110, v23
	global_load_dwordx4 v[172:175], v[172:173], off nt
	v_xor_b32_e32 v109, v109, v23
	global_load_dwordx4 v[176:179], v[176:177], off nt
	v_xor_b32_e32 v108, v108, v23
	v_xor_b32_e32 v107, v107, v23
	v_xor_b32_e32 v106, v106, v23
	v_xor_b32_e32 v105, v105, v23
	v_xor_b32_e32 v104, v104, v23
	v_xor_b32_e32 v103, v103, v23
	v_xor_b32_e32 v102, v102, v23
	v_xor_b32_e32 v101, v101, v23
	v_xor_b32_e32 v100, v100, v23
	v_xor_b32_e32 v7, v7, v23
	v_xor_b32_e32 v6, v6, v23
	v_lshl_add_u32 v113, v113, 4, v26
	v_lshl_add_u32 v112, v112, 4, v29
	v_lshl_add_u32 v111, v111, 4, v32
	v_lshl_add_u32 v110, v110, 4, v35
	v_lshl_add_u32 v109, v109, 4, v38
	v_lshl_add_u32 v108, v108, 4, v41
	v_lshl_add_u32 v107, v107, 4, v44
	v_lshl_add_u32 v106, v106, 4, v47
	v_lshl_add_u32 v105, v105, 4, v50
	v_lshl_add_u32 v104, v104, 4, v53
	v_lshl_add_u32 v103, v103, 4, v56
	v_lshl_add_u32 v102, v102, 4, v59
	v_lshl_add_u32 v101, v101, 4, v62
	v_lshl_add_u32 v100, v100, 4, v65
	v_lshl_add_u32 v7, v7, 4, v68
	v_lshl_add_u32 v6, v6, 4, v71
	s_ashr_i32 s75, s74, 31
	s_mov_b64 s[80:81], -1
	s_and_b64 vcc, exec, s[78:79]
	s_waitcnt vmcnt(15)
; #define GAS __attribute__((address_space(1)))
; #define LAS __attribute__((address_space(3)))
; __device__ __forceinline__ unsigned cvt_pk_bf16(float lo, float hi) { unsigned r; asm volatile("v_cvt_pk_bf16_f32 %0, %1, %2" : "=v"(r) : "v"(lo), "v"(hi)); return r; }
; __device__ __forceinline__ void conv_to_lds(const ConvJob& J, int tid, const f32x4 (&v)[16], LAS float* T) {
; #pragma unroll
;     for (int ii = 0; ii < 16; ++ii) { const int idx = tid + 512 * ii, k = idx >> 6, c4 = idx & 63; const int g = J.f8 ? ((k >> 4) & 7) : ((k >> 3) & 15);
;         *(LAS f32x4*)(T + k * 256 + 4 * (c4 ^ g)) = v[ii]; }
; }
; __device__ __forceinline__ void conv_from_lds(const ConvJob& J, int tid, const LAS float* T) {
;     ...
;         const int c = ((lane >> 2) & 7) + 8 * (lane >> 5);
; #pragma unroll
;         for (int it = 0; it < 8; ++it) { const int c4n = w * 8 + it, n = 4 * c4n + j; const LAS float* base = T + 4 * (c4n ^ c) + j + (8 * c) * 256;
;             u32x4 o; o.x = cvt_pk_bf16(base[0 * 256], base[1 * 256]); o.y = cvt_pk_bf16(base[2 * 256], base[3 * 256]); o.z = cvt_pk_bf16(base[4 * 256], base[5 * 256]); o.w = cvt_pk_bf16(base[6 * 256], base[7 * 256]);
;             *(GAS u32x4*)(J.WT + ((size_t)conv_dst_row(J.mode, n0 - J.ncol0 + n) * J.K + k0 + 8 * c) * 2) = o; }
	ds_write_b128 v113, v[114:117]
	s_waitcnt vmcnt(14)
	ds_write_b128 v112, v[118:121]
	s_waitcnt vmcnt(13)
	ds_write_b128 v111, v[122:125]
	s_waitcnt vmcnt(12)
	ds_write_b128 v110, v[126:129]
	s_waitcnt vmcnt(11)
	ds_write_b128 v109, v[130:133]
	s_waitcnt vmcnt(10)
	ds_write_b128 v108, v[134:137]
	s_waitcnt vmcnt(9)
	ds_write_b128 v107, v[138:141]
	s_waitcnt vmcnt(8)
	ds_write_b128 v106, v[142:145]
	s_waitcnt vmcnt(7)
	ds_write_b128 v105, v[146:149]
	s_waitcnt vmcnt(6)
	ds_write_b128 v104, v[150:153]
	s_waitcnt vmcnt(5)
	ds_write_b128 v103, v[154:157]
	s_waitcnt vmcnt(4)
	ds_write_b128 v102, v[158:161]
	s_waitcnt vmcnt(3)
	ds_write_b128 v101, v[164:167]
	s_waitcnt vmcnt(2)
	ds_write_b128 v100, v[168:171]
	s_waitcnt vmcnt(1)
	ds_write_b128 v7, v[172:175]
	s_waitcnt vmcnt(0)
	ds_write_b128 v6, v[176:179]
	s_waitcnt lgkmcnt(0)
	s_barrier
	s_cbranch_vccz .LBB0_1799
	ds_read2st64_b32 v[100:101], v88 offset1:4
	s_waitcnt lgkmcnt(0)
	v_cvt_pk_bf16_f32 v100, v100, v101
	ds_read2st64_b32 v[102:103], v88 offset0:8 offset1:12
	s_waitcnt lgkmcnt(0)
	v_cvt_pk_bf16_f32 v101, v102, v103
	ds_read2st64_b32 v[102:103], v88 offset0:16 offset1:20
	s_waitcnt lgkmcnt(0)
	v_cvt_pk_bf16_f32 v102, v102, v103
	ds_read2st64_b32 v[104:105], v88 offset0:24 offset1:28
	v_add_u32_e32 v106, s10, v72
	v_mov_b32_e32 v7, s75
	v_or_b32_e32 v6, s74, v2
	s_waitcnt lgkmcnt(0)
	v_cvt_pk_bf16_f32 v103, v104, v105
	v_ashrrev_i32_e32 v104, 31, v106
	v_mul_lo_u32 v107, s72, v104
	v_mad_u64_u32 v[104:105], s[12:13], s72, v106, v[6:7]
	v_mul_lo_u32 v106, s73, v106
	v_add3_u32 v105, v106, v105, v107
	v_lshl_add_u64 v[104:105], v[104:105], 1, s[76:77]
	global_store_dwordx4 v[104:105], v[100:103], off
	ds_read2st64_b32 v[100:101], v89 offset1:4
	v_add_u32_e32 v106, s10, v73
	s_waitcnt lgkmcnt(0)
	v_cvt_pk_bf16_f32 v100, v100, v101
	ds_read2st64_b32 v[102:103], v89 offset0:8 offset1:12
	s_waitcnt lgkmcnt(0)
	v_cvt_pk_bf16_f32 v101, v102, v103
	ds_read2st64_b32 v[102:103], v89 offset0:16 offset1:20
	s_waitcnt lgkmcnt(0)
	v_cvt_pk_bf16_f32 v102, v102, v103
	ds_read2st64_b32 v[104:105], v89 offset0:24 offset1:28
	s_waitcnt lgkmcnt(0)
	v_cvt_pk_bf16_f32 v103, v104, v105
	v_ashrrev_i32_e32 v104, 31, v106
	v_mul_lo_u32 v107, s72, v104
	v_mad_u64_u32 v[104:105], s[12:13], s72, v106, v[6:7]
	v_mul_lo_u32 v106, s73, v106
	v_add3_u32 v105, v106, v105, v107
	v_lshl_add_u64 v[104:105], v[104:105], 1, s[76:77]
	global_store_dwordx4 v[104:105], v[100:103], off
	ds_read2st64_b32 v[100:101], v90 offset1:4
	v_add_u32_e32 v106, s10, v74
	s_waitcnt lgkmcnt(0)
	v_cvt_pk_bf16_f32 v100, v100, v101
	ds_read2st64_b32 v[102:103], v90 offset0:8 offset1:12
	s_waitcnt lgkmcnt(0)
	v_cvt_pk_bf16_f32 v101, v102, v103
	ds_read2st64_b32 v[102:103], v90 offset0:16 offset1:20
	s_waitcnt lgkmcnt(0)
	v_cvt_pk_bf16_f32 v102, v102, v103
	ds_read2st64_b32 v[104:105], v90 offset0:24 offset1:28
	s_waitcnt lgkmcnt(0)
	v_cvt_pk_bf16_f32 v103, v104, v105
	v_ashrrev_i32_e32 v104, 31, v106
	v_mul_lo_u32 v107, s72, v104
	v_mad_u64_u32 v[104:105], s[12:13], s72, v106, v[6:7]
	v_mul_lo_u32 v106, s73, v106
	v_add3_u32 v105, v106, v105, v107
	v_lshl_add_u64 v[104:105], v[104:105], 1, s[76:77]
	global_store_dwordx4 v[104:105], v[100:103], off
	ds_read2st64_b32 v[100:101], v91 offset1:4
	v_add_u32_e32 v106, s10, v75
	s_waitcnt lgkmcnt(0)
	v_cvt_pk_bf16_f32 v100, v100, v101
	ds_read2st64_b32 v[102:103], v91 offset0:8 offset1:12
	s_waitcnt lgkmcnt(0)
	v_cvt_pk_bf16_f32 v101, v102, v103
	ds_read2st64_b32 v[102:103], v91 offset0:16 offset1:20
	s_waitcnt lgkmcnt(0)
	v_cvt_pk_bf16_f32 v102, v102, v103
	ds_read2st64_b32 v[104:105], v91 offset0:24 offset1:28
	s_waitcnt lgkmcnt(0)
	v_cvt_pk_bf16_f32 v103, v104, v105
	v_ashrrev_i32_e32 v104, 31, v106
	v_mul_lo_u32 v107, s72, v104
	v_mad_u64_u32 v[104:105], s[12:13], s72, v106, v[6:7]
	v_mul_lo_u32 v106, s73, v106
	v_add3_u32 v105, v106, v105, v107
	v_lshl_add_u64 v[104:105], v[104:105], 1, s[76:77]
	global_store_dwordx4 v[104:105], v[100:103], off
	ds_read2st64_b32 v[100:101], v92 offset1:4
	v_add_u32_e32 v106, s10, v76
	s_waitcnt lgkmcnt(0)
	v_cvt_pk_bf16_f32 v100, v100, v101
	ds_read2st64_b32 v[102:103], v92 offset0:8 offset1:12
	s_waitcnt lgkmcnt(0)
	v_cvt_pk_bf16_f32 v101, v102, v103
	ds_read2st64_b32 v[102:103], v92 offset0:16 offset1:20
	s_waitcnt lgkmcnt(0)
	v_cvt_pk_bf16_f32 v102, v102, v103
	ds_read2st64_b32 v[104:105], v92 offset0:24 offset1:28
	s_waitcnt lgkmcnt(0)
	v_cvt_pk_bf16_f32 v103, v104, v105
	v_ashrrev_i32_e32 v104, 31, v106
	v_mul_lo_u32 v107, s72, v104
	v_mad_u64_u32 v[104:105], s[12:13], s72, v106, v[6:7]
	v_mul_lo_u32 v106, s73, v106
	v_add3_u32 v105, v106, v105, v107
	v_lshl_add_u64 v[104:105], v[104:105], 1, s[76:77]
	global_store_dwordx4 v[104:105], v[100:103], off
	ds_read2st64_b32 v[100:101], v93 offset1:4
	v_add_u32_e32 v106, s10, v77
	s_waitcnt lgkmcnt(0)
	v_cvt_pk_bf16_f32 v100, v100, v101
	ds_read2st64_b32 v[102:103], v93 offset0:8 offset1:12
	s_waitcnt lgkmcnt(0)
	v_cvt_pk_bf16_f32 v101, v102, v103
	ds_read2st64_b32 v[102:103], v93 offset0:16 offset1:20
	s_waitcnt lgkmcnt(0)
	v_cvt_pk_bf16_f32 v102, v102, v103
	ds_read2st64_b32 v[104:105], v93 offset0:24 offset1:28
	s_waitcnt lgkmcnt(0)
	v_cvt_pk_bf16_f32 v103, v104, v105
	v_ashrrev_i32_e32 v104, 31, v106
	v_mul_lo_u32 v107, s72, v104
	v_mad_u64_u32 v[104:105], s[12:13], s72, v106, v[6:7]
	v_mul_lo_u32 v106, s73, v106
	v_add3_u32 v105, v106, v105, v107
	v_lshl_add_u64 v[104:105], v[104:105], 1, s[76:77]
	global_store_dwordx4 v[104:105], v[100:103], off
	ds_read2st64_b32 v[100:101], v94 offset1:4
	v_add_u32_e32 v106, s10, v78
	s_waitcnt lgkmcnt(0)
	v_cvt_pk_bf16_f32 v100, v100, v101
	ds_read2st64_b32 v[102:103], v94 offset0:8 offset1:12
	s_waitcnt lgkmcnt(0)
	v_cvt_pk_bf16_f32 v101, v102, v103
	ds_read2st64_b32 v[102:103], v94 offset0:16 offset1:20
	s_waitcnt lgkmcnt(0)
	v_cvt_pk_bf16_f32 v102, v102, v103
	ds_read2st64_b32 v[104:105], v94 offset0:24 offset1:28
	s_waitcnt lgkmcnt(0)
	v_cvt_pk_bf16_f32 v103, v104, v105
	v_ashrrev_i32_e32 v104, 31, v106
	v_mul_lo_u32 v107, s72, v104
	v_mad_u64_u32 v[104:105], s[12:13], s72, v106, v[6:7]
	v_mul_lo_u32 v106, s73, v106
	v_add3_u32 v105, v106, v105, v107
	v_lshl_add_u64 v[104:105], v[104:105], 1, s[76:77]
	global_store_dwordx4 v[104:105], v[100:103], off
	ds_read2st64_b32 v[100:101], v95 offset1:4
	s_mov_b64 s[80:81], 0
	s_waitcnt lgkmcnt(0)
	v_cvt_pk_bf16_f32 v100, v100, v101
	ds_read2st64_b32 v[102:103], v95 offset0:8 offset1:12
	s_waitcnt lgkmcnt(0)
	v_cvt_pk_bf16_f32 v101, v102, v103
	ds_read2st64_b32 v[102:103], v95 offset0:16 offset1:20
	s_waitcnt lgkmcnt(0)
	v_cvt_pk_bf16_f32 v102, v102, v103
	ds_read2st64_b32 v[104:105], v95 offset0:24 offset1:28
	s_waitcnt lgkmcnt(0)
	v_cvt_pk_bf16_f32 v103, v104, v105
	v_add_u32_e32 v104, s10, v79
	v_ashrrev_i32_e32 v105, 31, v104
	v_mul_lo_u32 v105, s72, v105
	v_mad_u64_u32 v[6:7], s[12:13], s72, v104, v[6:7]
	v_mul_lo_u32 v104, s73, v104
	v_add3_u32 v7, v104, v7, v105
	v_lshl_add_u64 v[6:7], v[6:7], 1, s[76:77]
	global_store_dwordx4 v[6:7], v[100:103], off

; #define GAS __attribute__((address_space(1)))
; #define LDS_BARRIER() asm volatile("s_waitcnt lgkmcnt(0)\n\ts_barrier" ::: "memory")
; __device__ __forceinline__ void conv8_load(const ConvJob& J, int tid, f32x4 (&v)[16]) {
;     const int nblk = J.ncols / 256, k0 = 128 * (J.item / nblk), n0 = J.ncol0 + 256 * (J.item % nblk);
;     const int lane = tid & 63, w = tid >> 6, kg = lane & 7, nq = lane >> 3;
;     const GAS float* p = J.W + (size_t)(k0 + 16 * kg) * J.N + n0 + 32 * w + 4 * nq;
; #pragma unroll
;     for (int j = 0; j < 16; ++j) v[j] = *(const GAS f32x4*)(p + (size_t)j * J.N);
; }
;     ...
;             for (;;) {
;                 if (tid == 0) *qw = __hip_atomic_fetch_add(ctr, 1u, RLX_AGENT);
;                 LDS_BARRIER();
;                 const int qd = q_hi + __builtin_amdgcn_readfirstlane((int)*qw);
;                 LDS_BARRIER();
;                 if (qd >= q_end) break;
;                 const ConvJob j = decode(qd < I_IN ? qd : qd + NB16); f32x4 v[16]; conv8_load(j, tid, v); conv8_store(j, tid, v); }
.LBB0_1836:
	v_cvt_f32_u32_e32 v2, s45
	s_sub_i32 s58, 0, s45
	s_abs_i32 s39, s44
	s_ashr_i32 s38, s44, 31
	v_rcp_iflag_f32_e32 v2, v2
	s_nop 0
	v_mul_f32_e32 v2, 0x4f7ffffe, v2
	v_cvt_u32_f32_e32 v2, v2
	s_nop 0
	v_readfirstlane_b32 s59, v2
	s_mul_i32 s58, s58, s59
	s_mul_hi_u32 s58, s59, s58
	s_add_i32 s59, s59, s58
	s_mul_hi_u32 s58, s39, s59
	s_mul_i32 s59, s58, s45
	s_sub_i32 s39, s39, s59
	s_add_i32 s60, s58, 1
	s_sub_i32 s59, s39, s45
	s_cmp_ge_u32 s39, s45
	s_cselect_b32 s58, s60, s58
	s_cselect_b32 s39, s59, s39
	s_add_i32 s59, s58, 1
	s_cmp_ge_u32 s39, s45
	s_cselect_b32 s39, s59, s58
	s_xor_b32 s39, s39, s38
	s_sub_i32 s39, s39, s38
	s_lshl_b32 s38, s39, 7
	s_mul_i32 s39, s39, s45
	s_sub_i32 s44, s44, s39
	v_or_b32_e32 v2, s38, v66
	s_ashr_i32 s39, s38, 31
	s_lshl_b32 s60, s44, 8
	s_mul_i32 s45, s42, s39
	v_mul_lo_u32 v4, s43, v2
	v_mad_u64_u32 v[2:3], s[58:59], s42, v2, 0
	s_add_i32 s44, s60, s57
	v_add3_u32 v3, v3, s45, v4
	v_lshl_add_u64 v[2:3], v[2:3], 2, s[40:41]
	s_ashr_i32 s45, s44, 31
	v_lshl_add_u64 v[2:3], s[44:45], 2, v[2:3]
	v_lshl_add_u64 v[2:3], v[68:69], 2, v[2:3]
	v_lshl_add_u64 v[2:3], v[2:3], 0, v[70:71]
	s_lshl_b64 s[40:41], s[42:43], 2
	v_lshl_add_u64 v[4:5], v[2:3], 0, s[40:41]
	global_load_dwordx4 v[26:29], v[2:3], off nt
	global_load_dwordx4 v[30:33], v[4:5], off nt
	v_lshl_add_u64 v[2:3], v[4:5], 0, s[40:41]
	v_lshl_add_u64 v[4:5], v[2:3], 0, s[40:41]
	global_load_dwordx4 v[58:61], v[2:3], off nt
	global_load_dwordx4 v[62:65], v[4:5], off nt
	v_lshl_add_u64 v[2:3], v[4:5], 0, s[40:41]
	v_lshl_add_u64 v[4:5], v[2:3], 0, s[40:41]
	global_load_dwordx4 v[42:45], v[2:3], off nt
	global_load_dwordx4 v[46:49], v[4:5], off nt
	v_lshl_add_u64 v[2:3], v[4:5], 0, s[40:41]
	global_load_dwordx4 v[34:37], v[2:3], off nt
	v_lshl_add_u64 v[2:3], v[2:3], 0, s[40:41]
	global_load_dwordx4 v[38:41], v[2:3], off nt
	v_lshl_add_u64 v[2:3], v[2:3], 0, s[40:41]
	global_load_dwordx4 v[6:9], v[2:3], off nt
	v_lshl_add_u64 v[2:3], v[2:3], 0, s[40:41]
	global_load_dwordx4 v[18:21], v[2:3], off nt
	v_lshl_add_u64 v[2:3], v[2:3], 0, s[40:41]
	global_load_dwordx4 v[50:53], v[2:3], off nt
	v_lshl_add_u64 v[2:3], v[2:3], 0, s[40:41]
	global_load_dwordx4 v[54:57], v[2:3], off nt
	v_lshl_add_u64 v[2:3], v[2:3], 0, s[40:41]
	global_load_dwordx4 v[10:13], v[2:3], off nt
	v_lshl_add_u64 v[2:3], v[2:3], 0, s[40:41]
	v_lshl_add_u64 v[14:15], v[2:3], 0, s[40:41]
	global_load_dwordx4 v[22:25], v[2:3], off nt
	v_add_u32_e32 v76, s60, v1
	global_load_dwordx4 v[2:5], v[14:15], off nt
	v_lshl_add_u64 v[14:15], v[14:15], 0, s[40:41]
	global_load_dwordx4 v[14:17], v[14:15], off nt
	s_cmp_lt_i32 s30, 2
	s_mov_b64 s[40:41], -1
	s_cbranch_scc1 .LBB0_1842
	s_cmp_gt_i32 s30, 2
	v_lshlrev_b32_e32 v78, 1, v76
	s_cbranch_scc0 .LBB0_1839
	v_and_or_b32 v77, v78, s50, v74
	s_mov_b64 s[40:41], 0
